# GEMM1 (even layers) gelu epilogue: packed f32 form arg=(K1 x^2+K0) x with folded constants, 5 plain/packed ops + 2 transcendentals per pair
# speedup vs baseline: 1.0053x; 1.0053x over previous
; __device__ __forceinline__ unsigned cvt_pk_bf16(float lo, float hi) { unsigned r; asm volatile("v_cvt_pk_bf16_f32 %0, %1, %2" : "=v"(r) : "v"(lo), "v"(hi)); return r; }
; __device__ __forceinline__ void st_wt16(void* p, u32x4 v) { asm volatile("global_store_dwordx4 %0, %1, off sc1\n\ts_nop 1" :: "v"(p), "v"(v) : "memory"); }
; __device__ __forceinline__ float gelu_tanh(float x) {
;     const float u2 = 1.5957691216057308f * (x + 0.044715f * x * x * x);
;     return x * __builtin_amdgcn_rcpf(1.0f + __expf(-u2));
; }
;     __device__ __forceinline__ void operator()(const f32x4 (&acc)[2][2][4][2], const Unit& u, int wr, int wc, int fr, int fq) const {
;     ...
; #pragma unroll
;         for (int ai = 0; ai < 2; ++ai)
; #pragma unroll
;             for (int m = 0; m < 4; ++m) {
;                 const int row = row0 + ai * HALF + m * 16;
;                 const float rs = rsv[ai * 4 + m];
;                 bf16* rowp = O + (size_t)row * ldc + col0;
; #pragma unroll
;                 for (int bj = 0; bj < 2; ++bj) {
;                     f32x4 v0 = acc[ai][bj][m][0] * rs, v1 = acc[ai][bj][m][1] * rs;
;                     if (gl) {
; #pragma unroll
;                         for (int j = 0; j < 4; ++j) { v0[j] = gelu_tanh(v0[j]); v1[j] = gelu_tanh(v1[j]); }
;                     }
;                     u32x4 w; w.x = cvt_pk_bf16(v0[0], v0[1]); w.y = cvt_pk_bf16(v0[2], v0[3]); w.z = cvt_pk_bf16(v1[0], v1[1]); w.w = cvt_pk_bf16(v1[2], v1[3]);
;                     if (ready && wt) st_wt16(rowp + bj * HALF, w); else *(u32x4*)(rowp + bj * HALF) = w;
.LBB0_236:
	v_lshrrev_b32_e32 v122, 1, v139
	s_lshl_b32 s0, s0, 8
	v_and_or_b32 v122, v122, 24, s0
	v_or_b32_e32 v122, s47, v122
	v_mov_b64_e32 v[124:125], s[8:9]
	v_cvt_pk_bf16_f32 v162, v162, v163
	v_cvt_pk_bf16_f32 v163, v128, v129
	v_cvt_pk_bf16_f32 v164, v164, v165
	v_cvt_pk_bf16_f32 v165, v126, v127
	v_mov_b32_e32 v126, v160
	v_mov_b32_e32 v127, v160
	v_mov_b32_e32 v161, v160
	v_ashrrev_i32_e32 v123, 31, v122
	v_mad_i64_i32 v[124:125], s[0:1], v140, s60, v[124:125]
	v_pk_mul_f32 v[120:121], v[120:121], v[126:127]
	v_pk_mul_f32 v[116:117], v[116:117], v[126:127]
	v_cndmask_b32_e64 v126, 0, 1, s[28:29]
	v_lshl_add_u64 v[124:125], v[122:123], 1, v[124:125]
	v_pk_mul_f32 v[118:119], v[118:119], v[160:161]
	v_cmp_ne_u32_e64 s[4:5], 1, v126
	s_andn2_b64 vcc, exec, s[28:29]
	v_pk_mul_f32 v[114:115], v[114:115], v[160:161]
	s_mov_b32 s61, 0x800000
	global_store_dwordx4 v[124:125], v[162:165], off
	s_cbranch_vccnz .LBB0_238
	s_mov_b32 s98, 0xbdd2d3e7
	s_mov_b32 s100, 0xc0135761
	v_pk_mul_f32 v[126:127], v[118:119], s[98:99] op_sel_hi:[1,0]
	v_pk_mul_f32 v[128:129], v[114:115], s[98:99] op_sel_hi:[1,0]
	v_pk_mul_f32 v[160:161], v[120:121], s[98:99] op_sel_hi:[1,0]
	v_pk_mul_f32 v[162:163], v[116:117], s[98:99] op_sel_hi:[1,0]
	v_pk_fma_f32 v[126:127], v[126:127], v[118:119], s[100:101] op_sel_hi:[1,1,0]
	v_pk_fma_f32 v[128:129], v[128:129], v[114:115], s[100:101] op_sel_hi:[1,1,0]
	v_pk_fma_f32 v[160:161], v[160:161], v[120:121], s[100:101] op_sel_hi:[1,1,0]
	v_pk_fma_f32 v[162:163], v[162:163], v[116:117], s[100:101] op_sel_hi:[1,1,0]
	v_pk_mul_f32 v[126:127], v[126:127], v[118:119]
	v_pk_mul_f32 v[128:129], v[128:129], v[114:115]
	v_pk_mul_f32 v[160:161], v[160:161], v[120:121]
	v_pk_mul_f32 v[162:163], v[162:163], v[116:117]
	v_exp_f32_e32 v126, v126
	v_exp_f32_e32 v127, v127
	v_exp_f32_e32 v128, v128
	v_exp_f32_e32 v129, v129
	v_exp_f32_e32 v160, v160
	v_exp_f32_e32 v161, v161
	v_exp_f32_e32 v162, v162
	v_exp_f32_e32 v163, v163
	v_add_f32_e32 v126, 1.0, v126
	v_add_f32_e32 v127, 1.0, v127
	v_add_f32_e32 v128, 1.0, v128
	v_add_f32_e32 v129, 1.0, v129
	v_add_f32_e32 v160, 1.0, v160
	v_add_f32_e32 v161, 1.0, v161
	v_add_f32_e32 v162, 1.0, v162
	v_add_f32_e32 v163, 1.0, v163
	v_rcp_f32_e32 v126, v126
	v_rcp_f32_e32 v127, v127
	v_rcp_f32_e32 v128, v128
	v_rcp_f32_e32 v129, v129
	v_rcp_f32_e32 v160, v160
	v_rcp_f32_e32 v161, v161
	v_rcp_f32_e32 v162, v162
	v_rcp_f32_e32 v163, v163
	v_pk_mul_f32 v[118:119], v[118:119], v[126:127]
	v_pk_mul_f32 v[114:115], v[114:115], v[128:129]
	v_pk_mul_f32 v[120:121], v[120:121], v[160:161]
	v_pk_mul_f32 v[116:117], v[116:117], v[162:163]
.LBB0_238:
	v_cvt_pk_bf16_f32 v118, v118, v119
	v_cvt_pk_bf16_f32 v119, v120, v121
	v_cvt_pk_bf16_f32 v120, v114, v115
	v_pk_mul_f32 v[112:113], v[112:113], v[156:157] op_sel_hi:[1,0]
	v_pk_mul_f32 v[110:111], v[110:111], v[156:157] op_sel_hi:[1,0]
	v_pk_mul_f32 v[108:109], v[108:109], v[156:157] op_sel_hi:[1,0]
	s_and_b64 vcc, exec, s[4:5]
	v_pk_mul_f32 v[114:115], v[106:107], v[156:157] op_sel_hi:[1,0]
	v_cvt_pk_bf16_f32 v121, v116, v117
	global_store_dwordx4 v[124:125], v[118:121], off offset:256
	s_cbranch_vccnz .LBB0_240
	s_mov_b32 s98, 0xbdd2d3e7
	s_mov_b32 s100, 0xc0135761
	v_pk_mul_f32 v[106:107], v[110:111], s[98:99] op_sel_hi:[1,0]
	v_pk_mul_f32 v[116:117], v[114:115], s[98:99] op_sel_hi:[1,0]
	v_pk_mul_f32 v[118:119], v[112:113], s[98:99] op_sel_hi:[1,0]
	v_pk_mul_f32 v[120:121], v[108:109], s[98:99] op_sel_hi:[1,0]
	v_pk_fma_f32 v[106:107], v[106:107], v[110:111], s[100:101] op_sel_hi:[1,1,0]
	v_pk_fma_f32 v[116:117], v[116:117], v[114:115], s[100:101] op_sel_hi:[1,1,0]
	v_pk_fma_f32 v[118:119], v[118:119], v[112:113], s[100:101] op_sel_hi:[1,1,0]
	v_pk_fma_f32 v[120:121], v[120:121], v[108:109], s[100:101] op_sel_hi:[1,1,0]
	v_pk_mul_f32 v[106:107], v[106:107], v[110:111]
	v_pk_mul_f32 v[116:117], v[116:117], v[114:115]
	v_pk_mul_f32 v[118:119], v[118:119], v[112:113]
	v_pk_mul_f32 v[120:121], v[120:121], v[108:109]
	v_exp_f32_e32 v106, v106
	v_exp_f32_e32 v107, v107
	v_exp_f32_e32 v116, v116
	v_exp_f32_e32 v117, v117
	v_exp_f32_e32 v118, v118
	v_exp_f32_e32 v119, v119
	v_exp_f32_e32 v120, v120
	v_exp_f32_e32 v121, v121
	v_add_f32_e32 v106, 1.0, v106
	v_add_f32_e32 v107, 1.0, v107
	v_add_f32_e32 v116, 1.0, v116
	v_add_f32_e32 v117, 1.0, v117
	v_add_f32_e32 v118, 1.0, v118
	v_add_f32_e32 v119, 1.0, v119
	v_add_f32_e32 v120, 1.0, v120
	v_add_f32_e32 v121, 1.0, v121
	v_rcp_f32_e32 v106, v106
	v_rcp_f32_e32 v107, v107
	v_rcp_f32_e32 v116, v116
	v_rcp_f32_e32 v117, v117
	v_rcp_f32_e32 v118, v118
	v_rcp_f32_e32 v119, v119
	v_rcp_f32_e32 v120, v120
	v_rcp_f32_e32 v121, v121
	v_pk_mul_f32 v[110:111], v[110:111], v[106:107]
	v_pk_mul_f32 v[114:115], v[114:115], v[116:117]
	v_pk_mul_f32 v[112:113], v[112:113], v[118:119]
	v_pk_mul_f32 v[108:109], v[108:109], v[120:121]
; __device__ __forceinline__ unsigned cvt_pk_bf16(float lo, float hi) { unsigned r; asm volatile("v_cvt_pk_bf16_f32 %0, %1, %2" : "=v"(r) : "v"(lo), "v"(hi)); return r; }
; __device__ __forceinline__ void st_wt16(void* p, u32x4 v) { asm volatile("global_store_dwordx4 %0, %1, off sc1\n\ts_nop 1" :: "v"(p), "v"(v) : "memory"); }
; __device__ __forceinline__ float gelu_tanh(float x) {
;     const float u2 = 1.5957691216057308f * (x + 0.044715f * x * x * x);
;     return x * __builtin_amdgcn_rcpf(1.0f + __expf(-u2));
; }
;     __device__ __forceinline__ void operator()(const f32x4 (&acc)[2][2][4][2], const Unit& u, int wr, int wc, int fr, int fq) const {
;     ...
; #pragma unroll
;         for (int ai = 0; ai < 2; ++ai)
; #pragma unroll
;             for (int m = 0; m < 4; ++m) {
;                 const int row = row0 + ai * HALF + m * 16;
;                 const float rs = rsv[ai * 4 + m];
;                 bf16* rowp = O + (size_t)row * ldc + col0;
; #pragma unroll
;                 for (int bj = 0; bj < 2; ++bj) {
;                     f32x4 v0 = acc[ai][bj][m][0] * rs, v1 = acc[ai][bj][m][1] * rs;
;                     if (gl) {
; #pragma unroll
;                         for (int j = 0; j < 4; ++j) { v0[j] = gelu_tanh(v0[j]); v1[j] = gelu_tanh(v1[j]); }
;                     }
;                     u32x4 w; w.x = cvt_pk_bf16(v0[0], v0[1]); w.y = cvt_pk_bf16(v0[2], v0[3]); w.z = cvt_pk_bf16(v1[0], v1[1]); w.w = cvt_pk_bf16(v1[2], v1[3]);
;                     if (ready && wt) st_wt16(rowp + bj * HALF, w); else *(u32x4*)(rowp + bj * HALF) = w;
.LBB0_240:
	v_mov_b64_e32 v[106:107], s[8:9]
	v_mov_b32_e32 v157, v156
	v_mad_i64_i32 v[106:107], s[0:1], v158, s60, v[106:107]
	v_cvt_pk_bf16_f32 v110, v110, v111
	v_cvt_pk_bf16_f32 v111, v112, v113
	v_cvt_pk_bf16_f32 v112, v114, v115
	v_cvt_pk_bf16_f32 v113, v108, v109
	v_mov_b32_e32 v108, v156
	v_mov_b32_e32 v109, v156
	v_lshl_add_u64 v[106:107], v[122:123], 1, v[106:107]
	v_pk_mul_f32 v[104:105], v[104:105], v[108:109]
	v_pk_mul_f32 v[102:103], v[102:103], v[156:157]
	v_pk_mul_f32 v[100:101], v[100:101], v[108:109]
	s_and_b64 vcc, exec, s[4:5]
	v_pk_mul_f32 v[98:99], v[98:99], v[156:157]
	global_store_dwordx4 v[106:107], v[110:113], off
	s_cbranch_vccnz .LBB0_242
	s_mov_b32 s98, 0xbdd2d3e7
	s_mov_b32 s100, 0xc0135761
	v_pk_mul_f32 v[108:109], v[102:103], s[98:99] op_sel_hi:[1,0]
	v_pk_mul_f32 v[110:111], v[98:99], s[98:99] op_sel_hi:[1,0]
	v_pk_mul_f32 v[112:113], v[104:105], s[98:99] op_sel_hi:[1,0]
	v_pk_mul_f32 v[114:115], v[100:101], s[98:99] op_sel_hi:[1,0]
	v_pk_fma_f32 v[108:109], v[108:109], v[102:103], s[100:101] op_sel_hi:[1,1,0]
	v_pk_fma_f32 v[110:111], v[110:111], v[98:99], s[100:101] op_sel_hi:[1,1,0]
	v_pk_fma_f32 v[112:113], v[112:113], v[104:105], s[100:101] op_sel_hi:[1,1,0]
	v_pk_fma_f32 v[114:115], v[114:115], v[100:101], s[100:101] op_sel_hi:[1,1,0]
	v_pk_mul_f32 v[108:109], v[108:109], v[102:103]
	v_pk_mul_f32 v[110:111], v[110:111], v[98:99]
	v_pk_mul_f32 v[112:113], v[112:113], v[104:105]
	v_pk_mul_f32 v[114:115], v[114:115], v[100:101]
	v_exp_f32_e32 v108, v108
	v_exp_f32_e32 v109, v109
	v_exp_f32_e32 v110, v110
	v_exp_f32_e32 v111, v111
	v_exp_f32_e32 v112, v112
	v_exp_f32_e32 v113, v113
	v_exp_f32_e32 v114, v114
	v_exp_f32_e32 v115, v115
	v_add_f32_e32 v108, 1.0, v108
	v_add_f32_e32 v109, 1.0, v109
	v_add_f32_e32 v110, 1.0, v110
	v_add_f32_e32 v111, 1.0, v111
	v_add_f32_e32 v112, 1.0, v112
	v_add_f32_e32 v113, 1.0, v113
	v_add_f32_e32 v114, 1.0, v114
	v_add_f32_e32 v115, 1.0, v115
	v_rcp_f32_e32 v108, v108
	v_rcp_f32_e32 v109, v109
	v_rcp_f32_e32 v110, v110
	v_rcp_f32_e32 v111, v111
	v_rcp_f32_e32 v112, v112
	v_rcp_f32_e32 v113, v113
	v_rcp_f32_e32 v114, v114
	v_rcp_f32_e32 v115, v115
	v_pk_mul_f32 v[102:103], v[102:103], v[108:109]
	v_pk_mul_f32 v[98:99], v[98:99], v[110:111]
	v_pk_mul_f32 v[104:105], v[104:105], v[112:113]
	v_pk_mul_f32 v[100:101], v[100:101], v[114:115]
.LBB0_242:
	v_cvt_pk_bf16_f32 v102, v102, v103
	v_cvt_pk_bf16_f32 v103, v104, v105
	v_cvt_pk_bf16_f32 v104, v98, v99
	v_pk_mul_f32 v[96:97], v[96:97], v[152:153] op_sel_hi:[1,0]
	v_pk_mul_f32 v[94:95], v[94:95], v[152:153] op_sel_hi:[1,0]
	v_pk_mul_f32 v[92:93], v[92:93], v[152:153] op_sel_hi:[1,0]
	s_and_b64 vcc, exec, s[4:5]
	v_pk_mul_f32 v[98:99], v[90:91], v[152:153] op_sel_hi:[1,0]
	v_cvt_pk_bf16_f32 v105, v100, v101
	global_store_dwordx4 v[106:107], v[102:105], off offset:256
	s_cbranch_vccnz .LBB0_244
	s_mov_b32 s98, 0xbdd2d3e7
	s_mov_b32 s100, 0xc0135761
	v_pk_mul_f32 v[90:91], v[94:95], s[98:99] op_sel_hi:[1,0]
	v_pk_mul_f32 v[100:101], v[98:99], s[98:99] op_sel_hi:[1,0]
	v_pk_mul_f32 v[102:103], v[96:97], s[98:99] op_sel_hi:[1,0]
	v_pk_mul_f32 v[104:105], v[92:93], s[98:99] op_sel_hi:[1,0]
	v_pk_fma_f32 v[90:91], v[90:91], v[94:95], s[100:101] op_sel_hi:[1,1,0]
	v_pk_fma_f32 v[100:101], v[100:101], v[98:99], s[100:101] op_sel_hi:[1,1,0]
	v_pk_fma_f32 v[102:103], v[102:103], v[96:97], s[100:101] op_sel_hi:[1,1,0]
	v_pk_fma_f32 v[104:105], v[104:105], v[92:93], s[100:101] op_sel_hi:[1,1,0]
	v_pk_mul_f32 v[90:91], v[90:91], v[94:95]
	v_pk_mul_f32 v[100:101], v[100:101], v[98:99]
	v_pk_mul_f32 v[102:103], v[102:103], v[96:97]
	v_pk_mul_f32 v[104:105], v[104:105], v[92:93]
	v_exp_f32_e32 v90, v90
	v_exp_f32_e32 v91, v91
	v_exp_f32_e32 v100, v100
	v_exp_f32_e32 v101, v101
	v_exp_f32_e32 v102, v102
	v_exp_f32_e32 v103, v103
	v_exp_f32_e32 v104, v104
	v_exp_f32_e32 v105, v105
	v_add_f32_e32 v90, 1.0, v90
	v_add_f32_e32 v91, 1.0, v91
	v_add_f32_e32 v100, 1.0, v100
	v_add_f32_e32 v101, 1.0, v101
	v_add_f32_e32 v102, 1.0, v102
	v_add_f32_e32 v103, 1.0, v103
	v_add_f32_e32 v104, 1.0, v104
	v_add_f32_e32 v105, 1.0, v105
	v_rcp_f32_e32 v90, v90
	v_rcp_f32_e32 v91, v91
	v_rcp_f32_e32 v100, v100
	v_rcp_f32_e32 v101, v101
	v_rcp_f32_e32 v102, v102
	v_rcp_f32_e32 v103, v103
	v_rcp_f32_e32 v104, v104
	v_rcp_f32_e32 v105, v105
	v_pk_mul_f32 v[94:95], v[94:95], v[90:91]
	v_pk_mul_f32 v[98:99], v[98:99], v[100:101]
	v_pk_mul_f32 v[96:97], v[96:97], v[102:103]
	v_pk_mul_f32 v[92:93], v[92:93], v[104:105]
.LBB0_244:
	v_mov_b64_e32 v[90:91], s[8:9]
	v_mov_b32_e32 v153, v152
	v_mad_i64_i32 v[90:91], s[0:1], v154, s60, v[90:91]
	v_cvt_pk_bf16_f32 v94, v94, v95
	v_cvt_pk_bf16_f32 v95, v96, v97
	v_cvt_pk_bf16_f32 v96, v98, v99
	v_cvt_pk_bf16_f32 v97, v92, v93
	v_mov_b32_e32 v92, v152
	v_mov_b32_e32 v93, v152
	v_lshl_add_u64 v[90:91], v[122:123], 1, v[90:91]
	v_pk_mul_f32 v[88:89], v[88:89], v[92:93]
	v_pk_mul_f32 v[86:87], v[86:87], v[152:153]
	v_pk_mul_f32 v[84:85], v[84:85], v[92:93]
	s_and_b64 vcc, exec, s[4:5]
	v_pk_mul_f32 v[82:83], v[82:83], v[152:153]
	global_store_dwordx4 v[90:91], v[94:97], off
	s_cbranch_vccnz .LBB0_246
	s_mov_b32 s98, 0xbdd2d3e7
	s_mov_b32 s100, 0xc0135761
	v_pk_mul_f32 v[92:93], v[86:87], s[98:99] op_sel_hi:[1,0]
	v_pk_mul_f32 v[94:95], v[82:83], s[98:99] op_sel_hi:[1,0]
	v_pk_mul_f32 v[96:97], v[88:89], s[98:99] op_sel_hi:[1,0]
	v_pk_mul_f32 v[98:99], v[84:85], s[98:99] op_sel_hi:[1,0]
	v_pk_fma_f32 v[92:93], v[92:93], v[86:87], s[100:101] op_sel_hi:[1,1,0]
	v_pk_fma_f32 v[94:95], v[94:95], v[82:83], s[100:101] op_sel_hi:[1,1,0]
	v_pk_fma_f32 v[96:97], v[96:97], v[88:89], s[100:101] op_sel_hi:[1,1,0]
	v_pk_fma_f32 v[98:99], v[98:99], v[84:85], s[100:101] op_sel_hi:[1,1,0]
	v_pk_mul_f32 v[92:93], v[92:93], v[86:87]
	v_pk_mul_f32 v[94:95], v[94:95], v[82:83]
	v_pk_mul_f32 v[96:97], v[96:97], v[88:89]
	v_pk_mul_f32 v[98:99], v[98:99], v[84:85]
	v_exp_f32_e32 v92, v92
	v_exp_f32_e32 v93, v93
	v_exp_f32_e32 v94, v94
	v_exp_f32_e32 v95, v95
	v_exp_f32_e32 v96, v96
	v_exp_f32_e32 v97, v97
	v_exp_f32_e32 v98, v98
	v_exp_f32_e32 v99, v99
	v_add_f32_e32 v92, 1.0, v92
	v_add_f32_e32 v93, 1.0, v93
	v_add_f32_e32 v94, 1.0, v94
	v_add_f32_e32 v95, 1.0, v95
	v_add_f32_e32 v96, 1.0, v96
	v_add_f32_e32 v97, 1.0, v97
	v_add_f32_e32 v98, 1.0, v98
	v_add_f32_e32 v99, 1.0, v99
	v_rcp_f32_e32 v92, v92
	v_rcp_f32_e32 v93, v93
	v_rcp_f32_e32 v94, v94
	v_rcp_f32_e32 v95, v95
	v_rcp_f32_e32 v96, v96
	v_rcp_f32_e32 v97, v97
	v_rcp_f32_e32 v98, v98
	v_rcp_f32_e32 v99, v99
	v_pk_mul_f32 v[86:87], v[86:87], v[92:93]
	v_pk_mul_f32 v[82:83], v[82:83], v[94:95]
	v_pk_mul_f32 v[88:89], v[88:89], v[96:97]
	v_pk_mul_f32 v[84:85], v[84:85], v[98:99]
; __device__ __forceinline__ unsigned cvt_pk_bf16(float lo, float hi) { unsigned r; asm volatile("v_cvt_pk_bf16_f32 %0, %1, %2" : "=v"(r) : "v"(lo), "v"(hi)); return r; }
; __device__ __forceinline__ void st_wt16(void* p, u32x4 v) { asm volatile("global_store_dwordx4 %0, %1, off sc1\n\ts_nop 1" :: "v"(p), "v"(v) : "memory"); }
; __device__ __forceinline__ float gelu_tanh(float x) {
;     const float u2 = 1.5957691216057308f * (x + 0.044715f * x * x * x);
;     return x * __builtin_amdgcn_rcpf(1.0f + __expf(-u2));
; }
;     __device__ __forceinline__ void operator()(const f32x4 (&acc)[2][2][4][2], const Unit& u, int wr, int wc, int fr, int fq) const {
;     ...
; #pragma unroll
;         for (int ai = 0; ai < 2; ++ai)
; #pragma unroll
;             for (int m = 0; m < 4; ++m) {
;                 const int row = row0 + ai * HALF + m * 16;
;                 const float rs = rsv[ai * 4 + m];
;                 bf16* rowp = O + (size_t)row * ldc + col0;
; #pragma unroll
;                 for (int bj = 0; bj < 2; ++bj) {
;                     f32x4 v0 = acc[ai][bj][m][0] * rs, v1 = acc[ai][bj][m][1] * rs;
;                     if (gl) {
; #pragma unroll
;                         for (int j = 0; j < 4; ++j) { v0[j] = gelu_tanh(v0[j]); v1[j] = gelu_tanh(v1[j]); }
;                     }
;                     u32x4 w; w.x = cvt_pk_bf16(v0[0], v0[1]); w.y = cvt_pk_bf16(v0[2], v0[3]); w.z = cvt_pk_bf16(v1[0], v1[1]); w.w = cvt_pk_bf16(v1[2], v1[3]);
;                     if (ready && wt) st_wt16(rowp + bj * HALF, w); else *(u32x4*)(rowp + bj * HALF) = w;
.LBB0_246:
	v_cvt_pk_bf16_f32 v86, v86, v87
	v_cvt_pk_bf16_f32 v87, v88, v89
	v_cvt_pk_bf16_f32 v88, v82, v83
	v_pk_mul_f32 v[80:81], v[80:81], v[148:149] op_sel_hi:[1,0]
	v_pk_mul_f32 v[78:79], v[78:79], v[148:149] op_sel_hi:[1,0]
	v_pk_mul_f32 v[76:77], v[76:77], v[148:149] op_sel_hi:[1,0]
	s_and_b64 vcc, exec, s[4:5]
	v_pk_mul_f32 v[82:83], v[74:75], v[148:149] op_sel_hi:[1,0]
	v_cvt_pk_bf16_f32 v89, v84, v85
	global_store_dwordx4 v[90:91], v[86:89], off offset:256
	s_cbranch_vccnz .LBB0_248
	s_mov_b32 s98, 0xbdd2d3e7
	s_mov_b32 s100, 0xc0135761
	v_pk_mul_f32 v[74:75], v[78:79], s[98:99] op_sel_hi:[1,0]
	v_pk_mul_f32 v[84:85], v[82:83], s[98:99] op_sel_hi:[1,0]
	v_pk_mul_f32 v[86:87], v[80:81], s[98:99] op_sel_hi:[1,0]
	v_pk_mul_f32 v[88:89], v[76:77], s[98:99] op_sel_hi:[1,0]
	v_pk_fma_f32 v[74:75], v[74:75], v[78:79], s[100:101] op_sel_hi:[1,1,0]
	v_pk_fma_f32 v[84:85], v[84:85], v[82:83], s[100:101] op_sel_hi:[1,1,0]
	v_pk_fma_f32 v[86:87], v[86:87], v[80:81], s[100:101] op_sel_hi:[1,1,0]
	v_pk_fma_f32 v[88:89], v[88:89], v[76:77], s[100:101] op_sel_hi:[1,1,0]
	v_pk_mul_f32 v[74:75], v[74:75], v[78:79]
	v_pk_mul_f32 v[84:85], v[84:85], v[82:83]
	v_pk_mul_f32 v[86:87], v[86:87], v[80:81]
	v_pk_mul_f32 v[88:89], v[88:89], v[76:77]
	v_exp_f32_e32 v74, v74
	v_exp_f32_e32 v75, v75
	v_exp_f32_e32 v84, v84
	v_exp_f32_e32 v85, v85
	v_exp_f32_e32 v86, v86
	v_exp_f32_e32 v87, v87
	v_exp_f32_e32 v88, v88
	v_exp_f32_e32 v89, v89
	v_add_f32_e32 v74, 1.0, v74
	v_add_f32_e32 v75, 1.0, v75
	v_add_f32_e32 v84, 1.0, v84
	v_add_f32_e32 v85, 1.0, v85
	v_add_f32_e32 v86, 1.0, v86
	v_add_f32_e32 v87, 1.0, v87
	v_add_f32_e32 v88, 1.0, v88
	v_add_f32_e32 v89, 1.0, v89
	v_rcp_f32_e32 v74, v74
	v_rcp_f32_e32 v75, v75
	v_rcp_f32_e32 v84, v84
	v_rcp_f32_e32 v85, v85
	v_rcp_f32_e32 v86, v86
	v_rcp_f32_e32 v87, v87
	v_rcp_f32_e32 v88, v88
	v_rcp_f32_e32 v89, v89
	v_pk_mul_f32 v[78:79], v[78:79], v[74:75]
	v_pk_mul_f32 v[82:83], v[82:83], v[84:85]
	v_pk_mul_f32 v[80:81], v[80:81], v[86:87]
	v_pk_mul_f32 v[76:77], v[76:77], v[88:89]
.LBB0_248:
	v_mov_b64_e32 v[74:75], s[8:9]
	v_mov_b32_e32 v149, v148
	v_mad_i64_i32 v[74:75], s[0:1], v150, s60, v[74:75]
	v_cvt_pk_bf16_f32 v78, v78, v79
	v_cvt_pk_bf16_f32 v79, v80, v81
	v_cvt_pk_bf16_f32 v80, v82, v83
	v_cvt_pk_bf16_f32 v81, v76, v77
	v_mov_b32_e32 v76, v148
	v_mov_b32_e32 v77, v148
	v_lshl_add_u64 v[74:75], v[122:123], 1, v[74:75]
	v_pk_mul_f32 v[72:73], v[72:73], v[76:77]
	v_pk_mul_f32 v[70:71], v[70:71], v[148:149]
	v_pk_mul_f32 v[68:69], v[68:69], v[76:77]
	s_and_b64 vcc, exec, s[4:5]
	v_pk_mul_f32 v[66:67], v[66:67], v[148:149]
	global_store_dwordx4 v[74:75], v[78:81], off
	s_cbranch_vccnz .LBB0_250
	s_mov_b32 s98, 0xbdd2d3e7
	s_mov_b32 s100, 0xc0135761
	v_pk_mul_f32 v[76:77], v[70:71], s[98:99] op_sel_hi:[1,0]
	v_pk_mul_f32 v[78:79], v[66:67], s[98:99] op_sel_hi:[1,0]
	v_pk_mul_f32 v[80:81], v[72:73], s[98:99] op_sel_hi:[1,0]
	v_pk_mul_f32 v[82:83], v[68:69], s[98:99] op_sel_hi:[1,0]
	v_pk_fma_f32 v[76:77], v[76:77], v[70:71], s[100:101] op_sel_hi:[1,1,0]
	v_pk_fma_f32 v[78:79], v[78:79], v[66:67], s[100:101] op_sel_hi:[1,1,0]
	v_pk_fma_f32 v[80:81], v[80:81], v[72:73], s[100:101] op_sel_hi:[1,1,0]
	v_pk_fma_f32 v[82:83], v[82:83], v[68:69], s[100:101] op_sel_hi:[1,1,0]
	v_pk_mul_f32 v[76:77], v[76:77], v[70:71]
	v_pk_mul_f32 v[78:79], v[78:79], v[66:67]
	v_pk_mul_f32 v[80:81], v[80:81], v[72:73]
	v_pk_mul_f32 v[82:83], v[82:83], v[68:69]
	v_exp_f32_e32 v76, v76
	v_exp_f32_e32 v77, v77
	v_exp_f32_e32 v78, v78
	v_exp_f32_e32 v79, v79
	v_exp_f32_e32 v80, v80
	v_exp_f32_e32 v81, v81
	v_exp_f32_e32 v82, v82
	v_exp_f32_e32 v83, v83
	v_add_f32_e32 v76, 1.0, v76
	v_add_f32_e32 v77, 1.0, v77
	v_add_f32_e32 v78, 1.0, v78
	v_add_f32_e32 v79, 1.0, v79
	v_add_f32_e32 v80, 1.0, v80
	v_add_f32_e32 v81, 1.0, v81
	v_add_f32_e32 v82, 1.0, v82
	v_add_f32_e32 v83, 1.0, v83
	v_rcp_f32_e32 v76, v76
	v_rcp_f32_e32 v77, v77
	v_rcp_f32_e32 v78, v78
	v_rcp_f32_e32 v79, v79
	v_rcp_f32_e32 v80, v80
	v_rcp_f32_e32 v81, v81
	v_rcp_f32_e32 v82, v82
	v_rcp_f32_e32 v83, v83
	v_pk_mul_f32 v[70:71], v[70:71], v[76:77]
	v_pk_mul_f32 v[66:67], v[66:67], v[78:79]
	v_pk_mul_f32 v[72:73], v[72:73], v[80:81]
	v_pk_mul_f32 v[68:69], v[68:69], v[82:83]
.LBB0_250:
	v_cvt_pk_bf16_f32 v70, v70, v71
	v_cvt_pk_bf16_f32 v71, v72, v73
	v_cvt_pk_bf16_f32 v72, v66, v67
	v_pk_mul_f32 v[62:63], v[62:63], v[146:147] op_sel_hi:[1,0]
	v_pk_mul_f32 v[60:61], v[60:61], v[146:147] op_sel_hi:[1,0]
	v_pk_mul_f32 v[58:59], v[58:59], v[146:147] op_sel_hi:[1,0]
	s_and_b64 vcc, exec, s[4:5]
	v_pk_mul_f32 v[66:67], v[56:57], v[146:147] op_sel_hi:[1,0]
	v_cvt_pk_bf16_f32 v73, v68, v69
	global_store_dwordx4 v[74:75], v[70:73], off offset:256
	s_cbranch_vccnz .LBB0_252
	s_mov_b32 s98, 0xbdd2d3e7
	s_mov_b32 s100, 0xc0135761
	v_pk_mul_f32 v[56:57], v[60:61], s[98:99] op_sel_hi:[1,0]
	v_pk_mul_f32 v[68:69], v[66:67], s[98:99] op_sel_hi:[1,0]
	v_pk_mul_f32 v[70:71], v[62:63], s[98:99] op_sel_hi:[1,0]
	v_pk_mul_f32 v[72:73], v[58:59], s[98:99] op_sel_hi:[1,0]
	v_pk_fma_f32 v[56:57], v[56:57], v[60:61], s[100:101] op_sel_hi:[1,1,0]
	v_pk_fma_f32 v[68:69], v[68:69], v[66:67], s[100:101] op_sel_hi:[1,1,0]
	v_pk_fma_f32 v[70:71], v[70:71], v[62:63], s[100:101] op_sel_hi:[1,1,0]
	v_pk_fma_f32 v[72:73], v[72:73], v[58:59], s[100:101] op_sel_hi:[1,1,0]
	v_pk_mul_f32 v[56:57], v[56:57], v[60:61]
	v_pk_mul_f32 v[68:69], v[68:69], v[66:67]
	v_pk_mul_f32 v[70:71], v[70:71], v[62:63]
	v_pk_mul_f32 v[72:73], v[72:73], v[58:59]
	v_exp_f32_e32 v56, v56
	v_exp_f32_e32 v57, v57
	v_exp_f32_e32 v68, v68
	v_exp_f32_e32 v69, v69
	v_exp_f32_e32 v70, v70
	v_exp_f32_e32 v71, v71
	v_exp_f32_e32 v72, v72
	v_exp_f32_e32 v73, v73
	v_add_f32_e32 v56, 1.0, v56
	v_add_f32_e32 v57, 1.0, v57
	v_add_f32_e32 v68, 1.0, v68
	v_add_f32_e32 v69, 1.0, v69
	v_add_f32_e32 v70, 1.0, v70
	v_add_f32_e32 v71, 1.0, v71
	v_add_f32_e32 v72, 1.0, v72
	v_add_f32_e32 v73, 1.0, v73
	v_rcp_f32_e32 v56, v56
	v_rcp_f32_e32 v57, v57
	v_rcp_f32_e32 v68, v68
	v_rcp_f32_e32 v69, v69
	v_rcp_f32_e32 v70, v70
	v_rcp_f32_e32 v71, v71
	v_rcp_f32_e32 v72, v72
	v_rcp_f32_e32 v73, v73
	v_pk_mul_f32 v[60:61], v[60:61], v[56:57]
	v_pk_mul_f32 v[66:67], v[66:67], v[68:69]
	v_pk_mul_f32 v[62:63], v[62:63], v[70:71]
	v_pk_mul_f32 v[58:59], v[58:59], v[72:73]
; __device__ __forceinline__ unsigned cvt_pk_bf16(float lo, float hi) { unsigned r; asm volatile("v_cvt_pk_bf16_f32 %0, %1, %2" : "=v"(r) : "v"(lo), "v"(hi)); return r; }
; __device__ __forceinline__ void st_wt16(void* p, u32x4 v) { asm volatile("global_store_dwordx4 %0, %1, off sc1\n\ts_nop 1" :: "v"(p), "v"(v) : "memory"); }
; __device__ __forceinline__ float gelu_tanh(float x) {
;     const float u2 = 1.5957691216057308f * (x + 0.044715f * x * x * x);
;     return x * __builtin_amdgcn_rcpf(1.0f + __expf(-u2));
; }
;     __device__ __forceinline__ void operator()(const f32x4 (&acc)[2][2][4][2], const Unit& u, int wr, int wc, int fr, int fq) const {
;     ...
; #pragma unroll
;         for (int ai = 0; ai < 2; ++ai)
; #pragma unroll
;             for (int m = 0; m < 4; ++m) {
;                 const int row = row0 + ai * HALF + m * 16;
;                 const float rs = rsv[ai * 4 + m];
;                 bf16* rowp = O + (size_t)row * ldc + col0;
; #pragma unroll
;                 for (int bj = 0; bj < 2; ++bj) {
;                     f32x4 v0 = acc[ai][bj][m][0] * rs, v1 = acc[ai][bj][m][1] * rs;
;                     if (gl) {
; #pragma unroll
;                         for (int j = 0; j < 4; ++j) { v0[j] = gelu_tanh(v0[j]); v1[j] = gelu_tanh(v1[j]); }
;                     }
;                     u32x4 w; w.x = cvt_pk_bf16(v0[0], v0[1]); w.y = cvt_pk_bf16(v0[2], v0[3]); w.z = cvt_pk_bf16(v1[0], v1[1]); w.w = cvt_pk_bf16(v1[2], v1[3]);
;                     if (ready && wt) st_wt16(rowp + bj * HALF, w); else *(u32x4*)(rowp + bj * HALF) = w;
.LBB0_252:
	v_add_u32_e32 v68, 0x80, v140
	v_mov_b64_e32 v[56:57], s[8:9]
	v_mov_b32_e32 v147, v146
	v_mad_i64_i32 v[56:57], s[0:1], v68, s60, v[56:57]
	v_cvt_pk_bf16_f32 v60, v60, v61
	v_cvt_pk_bf16_f32 v61, v62, v63
	v_cvt_pk_bf16_f32 v62, v66, v67
	v_cvt_pk_bf16_f32 v63, v58, v59
	v_mov_b32_e32 v58, v146
	v_mov_b32_e32 v59, v146
	v_lshl_add_u64 v[56:57], v[122:123], 1, v[56:57]
	v_pk_mul_f32 v[54:55], v[54:55], v[58:59]
	v_pk_mul_f32 v[52:53], v[52:53], v[146:147]
	v_pk_mul_f32 v[50:51], v[50:51], v[58:59]
	s_and_b64 vcc, exec, s[4:5]
	v_pk_mul_f32 v[48:49], v[48:49], v[146:147]
	global_store_dwordx4 v[56:57], v[60:63], off
	s_cbranch_vccnz .LBB0_254
	s_mov_b32 s98, 0xbdd2d3e7
	s_mov_b32 s100, 0xc0135761
	v_pk_mul_f32 v[58:59], v[52:53], s[98:99] op_sel_hi:[1,0]
	v_pk_mul_f32 v[60:61], v[48:49], s[98:99] op_sel_hi:[1,0]
	v_pk_mul_f32 v[62:63], v[54:55], s[98:99] op_sel_hi:[1,0]
	v_pk_mul_f32 v[66:67], v[50:51], s[98:99] op_sel_hi:[1,0]
	v_pk_fma_f32 v[58:59], v[58:59], v[52:53], s[100:101] op_sel_hi:[1,1,0]
	v_pk_fma_f32 v[60:61], v[60:61], v[48:49], s[100:101] op_sel_hi:[1,1,0]
	v_pk_fma_f32 v[62:63], v[62:63], v[54:55], s[100:101] op_sel_hi:[1,1,0]
	v_pk_fma_f32 v[66:67], v[66:67], v[50:51], s[100:101] op_sel_hi:[1,1,0]
	v_pk_mul_f32 v[58:59], v[58:59], v[52:53]
	v_pk_mul_f32 v[60:61], v[60:61], v[48:49]
	v_pk_mul_f32 v[62:63], v[62:63], v[54:55]
	v_pk_mul_f32 v[66:67], v[66:67], v[50:51]
	v_exp_f32_e32 v58, v58
	v_exp_f32_e32 v59, v59
	v_exp_f32_e32 v60, v60
	v_exp_f32_e32 v61, v61
	v_exp_f32_e32 v62, v62
	v_exp_f32_e32 v63, v63
	v_exp_f32_e32 v66, v66
	v_exp_f32_e32 v67, v67
	v_add_f32_e32 v58, 1.0, v58
	v_add_f32_e32 v59, 1.0, v59
	v_add_f32_e32 v60, 1.0, v60
	v_add_f32_e32 v61, 1.0, v61
	v_add_f32_e32 v62, 1.0, v62
	v_add_f32_e32 v63, 1.0, v63
	v_add_f32_e32 v66, 1.0, v66
	v_add_f32_e32 v67, 1.0, v67
	v_rcp_f32_e32 v58, v58
	v_rcp_f32_e32 v59, v59
	v_rcp_f32_e32 v60, v60
	v_rcp_f32_e32 v61, v61
	v_rcp_f32_e32 v62, v62
	v_rcp_f32_e32 v63, v63
	v_rcp_f32_e32 v66, v66
	v_rcp_f32_e32 v67, v67
	v_pk_mul_f32 v[52:53], v[52:53], v[58:59]
	v_pk_mul_f32 v[48:49], v[48:49], v[60:61]
	v_pk_mul_f32 v[54:55], v[54:55], v[62:63]
	v_pk_mul_f32 v[50:51], v[50:51], v[66:67]
.LBB0_254:
	v_cvt_pk_bf16_f32 v52, v52, v53
	v_cvt_pk_bf16_f32 v53, v54, v55
	v_cvt_pk_bf16_f32 v54, v48, v49
	v_pk_mul_f32 v[46:47], v[46:47], v[144:145] op_sel_hi:[1,0]
	v_pk_mul_f32 v[44:45], v[44:45], v[144:145] op_sel_hi:[1,0]
	v_pk_mul_f32 v[42:43], v[42:43], v[144:145] op_sel_hi:[1,0]
	s_and_b64 vcc, exec, s[4:5]
	v_pk_mul_f32 v[48:49], v[40:41], v[144:145] op_sel_hi:[1,0]
	v_cvt_pk_bf16_f32 v55, v50, v51
	global_store_dwordx4 v[56:57], v[52:55], off offset:256
	s_cbranch_vccnz .LBB0_256
	s_mov_b32 s98, 0xbdd2d3e7
	s_mov_b32 s100, 0xc0135761
	v_pk_mul_f32 v[40:41], v[44:45], s[98:99] op_sel_hi:[1,0]
	v_pk_mul_f32 v[50:51], v[48:49], s[98:99] op_sel_hi:[1,0]
	v_pk_mul_f32 v[52:53], v[46:47], s[98:99] op_sel_hi:[1,0]
	v_pk_mul_f32 v[54:55], v[42:43], s[98:99] op_sel_hi:[1,0]
	v_pk_fma_f32 v[40:41], v[40:41], v[44:45], s[100:101] op_sel_hi:[1,1,0]
	v_pk_fma_f32 v[50:51], v[50:51], v[48:49], s[100:101] op_sel_hi:[1,1,0]
	v_pk_fma_f32 v[52:53], v[52:53], v[46:47], s[100:101] op_sel_hi:[1,1,0]
	v_pk_fma_f32 v[54:55], v[54:55], v[42:43], s[100:101] op_sel_hi:[1,1,0]
	v_pk_mul_f32 v[40:41], v[40:41], v[44:45]
	v_pk_mul_f32 v[50:51], v[50:51], v[48:49]
	v_pk_mul_f32 v[52:53], v[52:53], v[46:47]
	v_pk_mul_f32 v[54:55], v[54:55], v[42:43]
	v_exp_f32_e32 v40, v40
	v_exp_f32_e32 v41, v41
	v_exp_f32_e32 v50, v50
	v_exp_f32_e32 v51, v51
	v_exp_f32_e32 v52, v52
	v_exp_f32_e32 v53, v53
	v_exp_f32_e32 v54, v54
	v_exp_f32_e32 v55, v55
	v_add_f32_e32 v40, 1.0, v40
	v_add_f32_e32 v41, 1.0, v41
	v_add_f32_e32 v50, 1.0, v50
	v_add_f32_e32 v51, 1.0, v51
	v_add_f32_e32 v52, 1.0, v52
	v_add_f32_e32 v53, 1.0, v53
	v_add_f32_e32 v54, 1.0, v54
	v_add_f32_e32 v55, 1.0, v55
	v_rcp_f32_e32 v40, v40
	v_rcp_f32_e32 v41, v41
	v_rcp_f32_e32 v50, v50
	v_rcp_f32_e32 v51, v51
	v_rcp_f32_e32 v52, v52
	v_rcp_f32_e32 v53, v53
	v_rcp_f32_e32 v54, v54
	v_rcp_f32_e32 v55, v55
	v_pk_mul_f32 v[44:45], v[44:45], v[40:41]
	v_pk_mul_f32 v[48:49], v[48:49], v[50:51]
	v_pk_mul_f32 v[46:47], v[46:47], v[52:53]
	v_pk_mul_f32 v[42:43], v[42:43], v[54:55]
.LBB0_256:
	v_add_u32_e32 v50, 0x90, v140
	v_mov_b64_e32 v[40:41], s[8:9]
	v_mov_b32_e32 v145, v144
	v_mad_i64_i32 v[40:41], s[0:1], v50, s60, v[40:41]
	v_cvt_pk_bf16_f32 v44, v44, v45
	v_cvt_pk_bf16_f32 v45, v46, v47
	v_cvt_pk_bf16_f32 v46, v48, v49
	v_cvt_pk_bf16_f32 v47, v42, v43
	v_mov_b32_e32 v42, v144
	v_mov_b32_e32 v43, v144
	v_lshl_add_u64 v[40:41], v[122:123], 1, v[40:41]
	v_pk_mul_f32 v[38:39], v[38:39], v[42:43]
	v_pk_mul_f32 v[36:37], v[36:37], v[144:145]
	v_pk_mul_f32 v[34:35], v[34:35], v[42:43]
	s_and_b64 vcc, exec, s[4:5]
	v_pk_mul_f32 v[32:33], v[32:33], v[144:145]
	global_store_dwordx4 v[40:41], v[44:47], off
	s_cbranch_vccnz .LBB0_258
	s_mov_b32 s98, 0xbdd2d3e7
	s_mov_b32 s100, 0xc0135761
	v_pk_mul_f32 v[42:43], v[36:37], s[98:99] op_sel_hi:[1,0]
	v_pk_mul_f32 v[44:45], v[32:33], s[98:99] op_sel_hi:[1,0]
	v_pk_mul_f32 v[46:47], v[38:39], s[98:99] op_sel_hi:[1,0]
	v_pk_mul_f32 v[48:49], v[34:35], s[98:99] op_sel_hi:[1,0]
	v_pk_fma_f32 v[42:43], v[42:43], v[36:37], s[100:101] op_sel_hi:[1,1,0]
	v_pk_fma_f32 v[44:45], v[44:45], v[32:33], s[100:101] op_sel_hi:[1,1,0]
	v_pk_fma_f32 v[46:47], v[46:47], v[38:39], s[100:101] op_sel_hi:[1,1,0]
	v_pk_fma_f32 v[48:49], v[48:49], v[34:35], s[100:101] op_sel_hi:[1,1,0]
	v_pk_mul_f32 v[42:43], v[42:43], v[36:37]
	v_pk_mul_f32 v[44:45], v[44:45], v[32:33]
	v_pk_mul_f32 v[46:47], v[46:47], v[38:39]
	v_pk_mul_f32 v[48:49], v[48:49], v[34:35]
	v_exp_f32_e32 v42, v42
	v_exp_f32_e32 v43, v43
	v_exp_f32_e32 v44, v44
	v_exp_f32_e32 v45, v45
	v_exp_f32_e32 v46, v46
	v_exp_f32_e32 v47, v47
	v_exp_f32_e32 v48, v48
	v_exp_f32_e32 v49, v49
	v_add_f32_e32 v42, 1.0, v42
	v_add_f32_e32 v43, 1.0, v43
	v_add_f32_e32 v44, 1.0, v44
	v_add_f32_e32 v45, 1.0, v45
	v_add_f32_e32 v46, 1.0, v46
	v_add_f32_e32 v47, 1.0, v47
	v_add_f32_e32 v48, 1.0, v48
	v_add_f32_e32 v49, 1.0, v49
	v_rcp_f32_e32 v42, v42
	v_rcp_f32_e32 v43, v43
	v_rcp_f32_e32 v44, v44
	v_rcp_f32_e32 v45, v45
	v_rcp_f32_e32 v46, v46
	v_rcp_f32_e32 v47, v47
	v_rcp_f32_e32 v48, v48
	v_rcp_f32_e32 v49, v49
	v_pk_mul_f32 v[36:37], v[36:37], v[42:43]
	v_pk_mul_f32 v[32:33], v[32:33], v[44:45]
	v_pk_mul_f32 v[38:39], v[38:39], v[46:47]
	v_pk_mul_f32 v[34:35], v[34:35], v[48:49]
; __device__ __forceinline__ unsigned cvt_pk_bf16(float lo, float hi) { unsigned r; asm volatile("v_cvt_pk_bf16_f32 %0, %1, %2" : "=v"(r) : "v"(lo), "v"(hi)); return r; }
; __device__ __forceinline__ void st_wt16(void* p, u32x4 v) { asm volatile("global_store_dwordx4 %0, %1, off sc1\n\ts_nop 1" :: "v"(p), "v"(v) : "memory"); }
; __device__ __forceinline__ float gelu_tanh(float x) {
;     const float u2 = 1.5957691216057308f * (x + 0.044715f * x * x * x);
;     return x * __builtin_amdgcn_rcpf(1.0f + __expf(-u2));
; }
;     __device__ __forceinline__ void operator()(const f32x4 (&acc)[2][2][4][2], const Unit& u, int wr, int wc, int fr, int fq) const {
;     ...
; #pragma unroll
;         for (int ai = 0; ai < 2; ++ai)
; #pragma unroll
;             for (int m = 0; m < 4; ++m) {
;                 const int row = row0 + ai * HALF + m * 16;
;                 const float rs = rsv[ai * 4 + m];
;                 bf16* rowp = O + (size_t)row * ldc + col0;
; #pragma unroll
;                 for (int bj = 0; bj < 2; ++bj) {
;                     f32x4 v0 = acc[ai][bj][m][0] * rs, v1 = acc[ai][bj][m][1] * rs;
;                     if (gl) {
; #pragma unroll
;                         for (int j = 0; j < 4; ++j) { v0[j] = gelu_tanh(v0[j]); v1[j] = gelu_tanh(v1[j]); }
;                     }
;                     u32x4 w; w.x = cvt_pk_bf16(v0[0], v0[1]); w.y = cvt_pk_bf16(v0[2], v0[3]); w.z = cvt_pk_bf16(v1[0], v1[1]); w.w = cvt_pk_bf16(v1[2], v1[3]);
;                     if (ready && wt) st_wt16(rowp + bj * HALF, w); else *(u32x4*)(rowp + bj * HALF) = w;
.LBB0_258:
	v_cvt_pk_bf16_f32 v36, v36, v37
	v_cvt_pk_bf16_f32 v37, v38, v39
	v_cvt_pk_bf16_f32 v38, v32, v33
	v_pk_mul_f32 v[30:31], v[30:31], v[142:143] op_sel_hi:[1,0]
	v_pk_mul_f32 v[28:29], v[28:29], v[142:143] op_sel_hi:[1,0]
	v_pk_mul_f32 v[26:27], v[26:27], v[142:143] op_sel_hi:[1,0]
	s_and_b64 vcc, exec, s[4:5]
	v_pk_mul_f32 v[32:33], v[24:25], v[142:143] op_sel_hi:[1,0]
	v_cvt_pk_bf16_f32 v39, v34, v35
	global_store_dwordx4 v[40:41], v[36:39], off offset:256
	s_cbranch_vccnz .LBB0_260
	s_mov_b32 s98, 0xbdd2d3e7
	s_mov_b32 s100, 0xc0135761
	v_pk_mul_f32 v[24:25], v[28:29], s[98:99] op_sel_hi:[1,0]
	v_pk_mul_f32 v[34:35], v[32:33], s[98:99] op_sel_hi:[1,0]
	v_pk_mul_f32 v[36:37], v[30:31], s[98:99] op_sel_hi:[1,0]
	v_pk_mul_f32 v[38:39], v[26:27], s[98:99] op_sel_hi:[1,0]
	v_pk_fma_f32 v[24:25], v[24:25], v[28:29], s[100:101] op_sel_hi:[1,1,0]
	v_pk_fma_f32 v[34:35], v[34:35], v[32:33], s[100:101] op_sel_hi:[1,1,0]
	v_pk_fma_f32 v[36:37], v[36:37], v[30:31], s[100:101] op_sel_hi:[1,1,0]
	v_pk_fma_f32 v[38:39], v[38:39], v[26:27], s[100:101] op_sel_hi:[1,1,0]
	v_pk_mul_f32 v[24:25], v[24:25], v[28:29]
	v_pk_mul_f32 v[34:35], v[34:35], v[32:33]
	v_pk_mul_f32 v[36:37], v[36:37], v[30:31]
	v_pk_mul_f32 v[38:39], v[38:39], v[26:27]
	v_exp_f32_e32 v24, v24
	v_exp_f32_e32 v25, v25
	v_exp_f32_e32 v34, v34
	v_exp_f32_e32 v35, v35
	v_exp_f32_e32 v36, v36
	v_exp_f32_e32 v37, v37
	v_exp_f32_e32 v38, v38
	v_exp_f32_e32 v39, v39
	v_add_f32_e32 v24, 1.0, v24
	v_add_f32_e32 v25, 1.0, v25
	v_add_f32_e32 v34, 1.0, v34
	v_add_f32_e32 v35, 1.0, v35
	v_add_f32_e32 v36, 1.0, v36
	v_add_f32_e32 v37, 1.0, v37
	v_add_f32_e32 v38, 1.0, v38
	v_add_f32_e32 v39, 1.0, v39
	v_rcp_f32_e32 v24, v24
	v_rcp_f32_e32 v25, v25
	v_rcp_f32_e32 v34, v34
	v_rcp_f32_e32 v35, v35
	v_rcp_f32_e32 v36, v36
	v_rcp_f32_e32 v37, v37
	v_rcp_f32_e32 v38, v38
	v_rcp_f32_e32 v39, v39
	v_pk_mul_f32 v[28:29], v[28:29], v[24:25]
	v_pk_mul_f32 v[32:33], v[32:33], v[34:35]
	v_pk_mul_f32 v[30:31], v[30:31], v[36:37]
	v_pk_mul_f32 v[26:27], v[26:27], v[38:39]
.LBB0_260:
	v_add_u32_e32 v34, 0xa0, v140
	v_mov_b64_e32 v[24:25], s[8:9]
	v_mov_b32_e32 v143, v142
	v_mad_i64_i32 v[24:25], s[0:1], v34, s60, v[24:25]
	v_cvt_pk_bf16_f32 v28, v28, v29
	v_cvt_pk_bf16_f32 v29, v30, v31
	v_cvt_pk_bf16_f32 v30, v32, v33
	v_cvt_pk_bf16_f32 v31, v26, v27
	v_mov_b32_e32 v26, v142
	v_mov_b32_e32 v27, v142
	v_lshl_add_u64 v[24:25], v[122:123], 1, v[24:25]
	v_pk_mul_f32 v[22:23], v[22:23], v[26:27]
	v_pk_mul_f32 v[20:21], v[20:21], v[142:143]
	v_pk_mul_f32 v[18:19], v[18:19], v[26:27]
	s_and_b64 vcc, exec, s[4:5]
	v_pk_mul_f32 v[16:17], v[16:17], v[142:143]
	global_store_dwordx4 v[24:25], v[28:31], off
	s_cbranch_vccnz .LBB0_262
	s_mov_b32 s98, 0xbdd2d3e7
	s_mov_b32 s100, 0xc0135761
	v_pk_mul_f32 v[26:27], v[20:21], s[98:99] op_sel_hi:[1,0]
	v_pk_mul_f32 v[28:29], v[16:17], s[98:99] op_sel_hi:[1,0]
	v_pk_mul_f32 v[30:31], v[22:23], s[98:99] op_sel_hi:[1,0]
	v_pk_mul_f32 v[32:33], v[18:19], s[98:99] op_sel_hi:[1,0]
	v_pk_fma_f32 v[26:27], v[26:27], v[20:21], s[100:101] op_sel_hi:[1,1,0]
	v_pk_fma_f32 v[28:29], v[28:29], v[16:17], s[100:101] op_sel_hi:[1,1,0]
	v_pk_fma_f32 v[30:31], v[30:31], v[22:23], s[100:101] op_sel_hi:[1,1,0]
	v_pk_fma_f32 v[32:33], v[32:33], v[18:19], s[100:101] op_sel_hi:[1,1,0]
	v_pk_mul_f32 v[26:27], v[26:27], v[20:21]
	v_pk_mul_f32 v[28:29], v[28:29], v[16:17]
	v_pk_mul_f32 v[30:31], v[30:31], v[22:23]
	v_pk_mul_f32 v[32:33], v[32:33], v[18:19]
	v_exp_f32_e32 v26, v26
	v_exp_f32_e32 v27, v27
	v_exp_f32_e32 v28, v28
	v_exp_f32_e32 v29, v29
	v_exp_f32_e32 v30, v30
	v_exp_f32_e32 v31, v31
	v_exp_f32_e32 v32, v32
	v_exp_f32_e32 v33, v33
	v_add_f32_e32 v26, 1.0, v26
	v_add_f32_e32 v27, 1.0, v27
	v_add_f32_e32 v28, 1.0, v28
	v_add_f32_e32 v29, 1.0, v29
	v_add_f32_e32 v30, 1.0, v30
	v_add_f32_e32 v31, 1.0, v31
	v_add_f32_e32 v32, 1.0, v32
	v_add_f32_e32 v33, 1.0, v33
	v_rcp_f32_e32 v26, v26
	v_rcp_f32_e32 v27, v27
	v_rcp_f32_e32 v28, v28
	v_rcp_f32_e32 v29, v29
	v_rcp_f32_e32 v30, v30
	v_rcp_f32_e32 v31, v31
	v_rcp_f32_e32 v32, v32
	v_rcp_f32_e32 v33, v33
	v_pk_mul_f32 v[20:21], v[20:21], v[26:27]
	v_pk_mul_f32 v[16:17], v[16:17], v[28:29]
	v_pk_mul_f32 v[22:23], v[22:23], v[30:31]
	v_pk_mul_f32 v[18:19], v[18:19], v[32:33]
; __device__ __forceinline__ unsigned cvt_pk_bf16(float lo, float hi) { unsigned r; asm volatile("v_cvt_pk_bf16_f32 %0, %1, %2" : "=v"(r) : "v"(lo), "v"(hi)); return r; }
; __device__ __forceinline__ void st_wt16(void* p, u32x4 v) { asm volatile("global_store_dwordx4 %0, %1, off sc1\n\ts_nop 1" :: "v"(p), "v"(v) : "memory"); }
; __device__ __forceinline__ float gelu_tanh(float x) {
;     const float u2 = 1.5957691216057308f * (x + 0.044715f * x * x * x);
;     return x * __builtin_amdgcn_rcpf(1.0f + __expf(-u2));
; }
;     __device__ __forceinline__ void operator()(const f32x4 (&acc)[2][2][4][2], const Unit& u, int wr, int wc, int fr, int fq) const {
;     ...
; #pragma unroll
;         for (int ai = 0; ai < 2; ++ai)
; #pragma unroll
;             for (int m = 0; m < 4; ++m) {
;                 const int row = row0 + ai * HALF + m * 16;
;                 const float rs = rsv[ai * 4 + m];
;                 bf16* rowp = O + (size_t)row * ldc + col0;
; #pragma unroll
;                 for (int bj = 0; bj < 2; ++bj) {
;                     f32x4 v0 = acc[ai][bj][m][0] * rs, v1 = acc[ai][bj][m][1] * rs;
;                     if (gl) {
; #pragma unroll
;                         for (int j = 0; j < 4; ++j) { v0[j] = gelu_tanh(v0[j]); v1[j] = gelu_tanh(v1[j]); }
;                     }
;                     u32x4 w; w.x = cvt_pk_bf16(v0[0], v0[1]); w.y = cvt_pk_bf16(v0[2], v0[3]); w.z = cvt_pk_bf16(v1[0], v1[1]); w.w = cvt_pk_bf16(v1[2], v1[3]);
;                     if (ready && wt) st_wt16(rowp + bj * HALF, w); else *(u32x4*)(rowp + bj * HALF) = w;
.LBB0_262:
	v_cvt_pk_bf16_f32 v20, v20, v21
	v_cvt_pk_bf16_f32 v21, v22, v23
	v_cvt_pk_bf16_f32 v22, v16, v17
	v_pk_mul_f32 v[14:15], v[14:15], v[138:139] op_sel_hi:[1,0]
	v_pk_mul_f32 v[12:13], v[12:13], v[138:139] op_sel_hi:[1,0]
	v_pk_mul_f32 v[10:11], v[10:11], v[138:139] op_sel_hi:[1,0]
	s_and_b64 vcc, exec, s[4:5]
	v_pk_mul_f32 v[16:17], v[8:9], v[138:139] op_sel_hi:[1,0]
	v_cvt_pk_bf16_f32 v23, v18, v19
	global_store_dwordx4 v[24:25], v[20:23], off offset:256
	s_cbranch_vccnz .LBB0_264
	s_mov_b32 s98, 0xbdd2d3e7
	s_mov_b32 s100, 0xc0135761
	v_pk_mul_f32 v[8:9], v[12:13], s[98:99] op_sel_hi:[1,0]
	v_pk_mul_f32 v[18:19], v[16:17], s[98:99] op_sel_hi:[1,0]
	v_pk_mul_f32 v[20:21], v[14:15], s[98:99] op_sel_hi:[1,0]
	v_pk_mul_f32 v[22:23], v[10:11], s[98:99] op_sel_hi:[1,0]
	v_pk_fma_f32 v[8:9], v[8:9], v[12:13], s[100:101] op_sel_hi:[1,1,0]
	v_pk_fma_f32 v[18:19], v[18:19], v[16:17], s[100:101] op_sel_hi:[1,1,0]
	v_pk_fma_f32 v[20:21], v[20:21], v[14:15], s[100:101] op_sel_hi:[1,1,0]
	v_pk_fma_f32 v[22:23], v[22:23], v[10:11], s[100:101] op_sel_hi:[1,1,0]
	v_pk_mul_f32 v[8:9], v[8:9], v[12:13]
	v_pk_mul_f32 v[18:19], v[18:19], v[16:17]
	v_pk_mul_f32 v[20:21], v[20:21], v[14:15]
	v_pk_mul_f32 v[22:23], v[22:23], v[10:11]
	v_exp_f32_e32 v8, v8
	v_exp_f32_e32 v9, v9
	v_exp_f32_e32 v18, v18
	v_exp_f32_e32 v19, v19
	v_exp_f32_e32 v20, v20
	v_exp_f32_e32 v21, v21
	v_exp_f32_e32 v22, v22
	v_exp_f32_e32 v23, v23
	v_add_f32_e32 v8, 1.0, v8
	v_add_f32_e32 v9, 1.0, v9
	v_add_f32_e32 v18, 1.0, v18
	v_add_f32_e32 v19, 1.0, v19
	v_add_f32_e32 v20, 1.0, v20
	v_add_f32_e32 v21, 1.0, v21
	v_add_f32_e32 v22, 1.0, v22
	v_add_f32_e32 v23, 1.0, v23
	v_rcp_f32_e32 v8, v8
	v_rcp_f32_e32 v9, v9
	v_rcp_f32_e32 v18, v18
	v_rcp_f32_e32 v19, v19
	v_rcp_f32_e32 v20, v20
	v_rcp_f32_e32 v21, v21
	v_rcp_f32_e32 v22, v22
	v_rcp_f32_e32 v23, v23
	v_pk_mul_f32 v[12:13], v[12:13], v[8:9]
	v_pk_mul_f32 v[16:17], v[16:17], v[18:19]
	v_pk_mul_f32 v[14:15], v[14:15], v[20:21]
	v_pk_mul_f32 v[10:11], v[10:11], v[22:23]
.LBB0_264:
	v_add_u32_e32 v18, 0xb0, v140
	v_mov_b64_e32 v[8:9], s[8:9]
	v_mov_b32_e32 v139, v138
	v_mad_i64_i32 v[8:9], s[0:1], v18, s60, v[8:9]
	v_cvt_pk_bf16_f32 v12, v12, v13
	v_cvt_pk_bf16_f32 v13, v14, v15
	v_cvt_pk_bf16_f32 v14, v16, v17
	v_cvt_pk_bf16_f32 v15, v10, v11
	v_mov_b32_e32 v10, v138
	v_mov_b32_e32 v11, v138
	v_lshl_add_u64 v[8:9], v[122:123], 1, v[8:9]
	v_pk_mul_f32 v[6:7], v[6:7], v[10:11]
	v_pk_mul_f32 v[4:5], v[4:5], v[138:139]
	v_pk_mul_f32 v[2:3], v[2:3], v[10:11]
	s_and_b64 vcc, exec, s[4:5]
	v_pk_mul_f32 v[0:1], v[0:1], v[138:139]
	global_store_dwordx4 v[8:9], v[12:15], off
	s_cbranch_vccnz .LBB0_266
	s_mov_b32 s98, 0xbdd2d3e7
	s_mov_b32 s100, 0xc0135761
	v_pk_mul_f32 v[10:11], v[4:5], s[98:99] op_sel_hi:[1,0]
	v_pk_mul_f32 v[12:13], v[0:1], s[98:99] op_sel_hi:[1,0]
	v_pk_mul_f32 v[14:15], v[6:7], s[98:99] op_sel_hi:[1,0]
	v_pk_mul_f32 v[16:17], v[2:3], s[98:99] op_sel_hi:[1,0]
	v_pk_fma_f32 v[10:11], v[10:11], v[4:5], s[100:101] op_sel_hi:[1,1,0]
	v_pk_fma_f32 v[12:13], v[12:13], v[0:1], s[100:101] op_sel_hi:[1,1,0]
	v_pk_fma_f32 v[14:15], v[14:15], v[6:7], s[100:101] op_sel_hi:[1,1,0]
	v_pk_fma_f32 v[16:17], v[16:17], v[2:3], s[100:101] op_sel_hi:[1,1,0]
	v_pk_mul_f32 v[10:11], v[10:11], v[4:5]
	v_pk_mul_f32 v[12:13], v[12:13], v[0:1]
	v_pk_mul_f32 v[14:15], v[14:15], v[6:7]
	v_pk_mul_f32 v[16:17], v[16:17], v[2:3]
	v_exp_f32_e32 v10, v10
	v_exp_f32_e32 v11, v11
	v_exp_f32_e32 v12, v12
	v_exp_f32_e32 v13, v13
	v_exp_f32_e32 v14, v14
	v_exp_f32_e32 v15, v15
	v_exp_f32_e32 v16, v16
	v_exp_f32_e32 v17, v17
	v_add_f32_e32 v10, 1.0, v10
	v_add_f32_e32 v11, 1.0, v11
	v_add_f32_e32 v12, 1.0, v12
	v_add_f32_e32 v13, 1.0, v13
	v_add_f32_e32 v14, 1.0, v14
	v_add_f32_e32 v15, 1.0, v15
	v_add_f32_e32 v16, 1.0, v16
	v_add_f32_e32 v17, 1.0, v17
	v_rcp_f32_e32 v10, v10
	v_rcp_f32_e32 v11, v11
	v_rcp_f32_e32 v12, v12
	v_rcp_f32_e32 v13, v13
	v_rcp_f32_e32 v14, v14
	v_rcp_f32_e32 v15, v15
	v_rcp_f32_e32 v16, v16
	v_rcp_f32_e32 v17, v17
	v_pk_mul_f32 v[4:5], v[4:5], v[10:11]
	v_pk_mul_f32 v[0:1], v[0:1], v[12:13]
	v_pk_mul_f32 v[6:7], v[6:7], v[14:15]
	v_pk_mul_f32 v[2:3], v[2:3], v[16:17]

; __device__ __forceinline__ unsigned cvt_pk_bf16(float lo, float hi) { unsigned r; asm volatile("v_cvt_pk_bf16_f32 %0, %1, %2" : "=v"(r) : "v"(lo), "v"(hi)); return r; }
; __device__ __forceinline__ void st_wt16(void* p, u32x4 v) { asm volatile("global_store_dwordx4 %0, %1, off sc1\n\ts_nop 1" :: "v"(p), "v"(v) : "memory"); }
; __device__ __forceinline__ float gelu_tanh(float x) {
;     const float u2 = 1.5957691216057308f * (x + 0.044715f * x * x * x);
;     return x * __builtin_amdgcn_rcpf(1.0f + __expf(-u2));
; }
;     __device__ __forceinline__ void operator()(const f32x4 (&acc)[2][2][4][2], const Unit& u, int wr, int wc, int fr, int fq) const {
;     ...
; #pragma unroll
;         for (int ai = 0; ai < 2; ++ai)
; #pragma unroll
;             for (int m = 0; m < 4; ++m) {
;                 const int row = row0 + ai * HALF + m * 16;
;                 const float rs = rsv[ai * 4 + m];
;                 bf16* rowp = O + (size_t)row * ldc + col0;
; #pragma unroll
;                 for (int bj = 0; bj < 2; ++bj) {
;                     f32x4 v0 = acc[ai][bj][m][0] * rs, v1 = acc[ai][bj][m][1] * rs;
;                     if (gl) {
; #pragma unroll
;                         for (int j = 0; j < 4; ++j) { v0[j] = gelu_tanh(v0[j]); v1[j] = gelu_tanh(v1[j]); }
;                     }
;                     u32x4 w; w.x = cvt_pk_bf16(v0[0], v0[1]); w.y = cvt_pk_bf16(v0[2], v0[3]); w.z = cvt_pk_bf16(v1[0], v1[1]); w.w = cvt_pk_bf16(v1[2], v1[3]);
;                     if (ready && wt) st_wt16(rowp + bj * HALF, w); else *(u32x4*)(rowp + bj * HALF) = w;
.LBB0_307:
	s_lshl_b32 s1, s4, 8
	v_lshrrev_b32_e32 v122, 1, v139
	s_lshl_b32 s0, s0, 8
	s_add_i32 s1, s1, s43
	v_and_or_b32 v122, v122, 24, s0
	v_and_or_b32 v64, v139, 15, s1
	v_or_b32_e32 v122, s44, v122
	v_mov_b64_e32 v[124:125], s[8:9]
	v_ashrrev_i32_e32 v123, 31, v122
	v_mad_i64_i32 v[124:125], s[0:1], v64, s60, v[124:125]
	v_cvt_pk_bf16_f32 v130, v130, v131
	v_cvt_pk_bf16_f32 v131, v128, v129
	v_cvt_pk_bf16_f32 v132, v132, v133
	v_cvt_pk_bf16_f32 v133, v126, v127
	v_cndmask_b32_e64 v126, 0, 1, s[24:25]
	v_lshl_add_u64 v[124:125], v[122:123], 1, v[124:125]
	v_pk_mul_f32 v[120:121], v[120:121], s[10:11] op_sel_hi:[1,0]
	v_pk_mul_f32 v[118:119], v[118:119], s[10:11] op_sel_hi:[1,0]
	v_pk_mul_f32 v[116:117], v[116:117], s[10:11] op_sel_hi:[1,0]
	v_cmp_ne_u32_e64 s[4:5], 1, v126
	s_andn2_b64 vcc, exec, s[24:25]
	v_pk_mul_f32 v[114:115], v[114:115], s[10:11] op_sel_hi:[1,0]
	v_mov_b32_e32 v226, v216
	v_mov_b64_e32 v[228:229], 0x1e8481
	v_mov_b32_e32 v227, v217
	global_store_dwordx4 v[124:125], v[130:133], off
	s_cbranch_vccnz .LBB0_309
	s_mov_b32 s98, 0xbdd2d3e7
	s_mov_b32 s100, 0xc0135761
	v_pk_mul_f32 v[126:127], v[118:119], s[98:99] op_sel_hi:[1,0]
	v_pk_mul_f32 v[128:129], v[114:115], s[98:99] op_sel_hi:[1,0]
	v_pk_mul_f32 v[130:131], v[120:121], s[98:99] op_sel_hi:[1,0]
	v_pk_mul_f32 v[132:133], v[116:117], s[98:99] op_sel_hi:[1,0]
	v_pk_fma_f32 v[126:127], v[126:127], v[118:119], s[100:101] op_sel_hi:[1,1,0]
	v_pk_fma_f32 v[128:129], v[128:129], v[114:115], s[100:101] op_sel_hi:[1,1,0]
	v_pk_fma_f32 v[130:131], v[130:131], v[120:121], s[100:101] op_sel_hi:[1,1,0]
	v_pk_fma_f32 v[132:133], v[132:133], v[116:117], s[100:101] op_sel_hi:[1,1,0]
	v_pk_mul_f32 v[126:127], v[126:127], v[118:119]
	v_pk_mul_f32 v[128:129], v[128:129], v[114:115]
	v_pk_mul_f32 v[130:131], v[130:131], v[120:121]
	v_pk_mul_f32 v[132:133], v[132:133], v[116:117]
	v_exp_f32_e32 v126, v126
	v_exp_f32_e32 v127, v127
	v_exp_f32_e32 v128, v128
	v_exp_f32_e32 v129, v129
	v_exp_f32_e32 v130, v130
	v_exp_f32_e32 v131, v131
	v_exp_f32_e32 v132, v132
	v_exp_f32_e32 v133, v133
	v_add_f32_e32 v126, 1.0, v126
	v_add_f32_e32 v127, 1.0, v127
	v_add_f32_e32 v128, 1.0, v128
	v_add_f32_e32 v129, 1.0, v129
	v_add_f32_e32 v130, 1.0, v130
	v_add_f32_e32 v131, 1.0, v131
	v_add_f32_e32 v132, 1.0, v132
	v_add_f32_e32 v133, 1.0, v133
	v_rcp_f32_e32 v126, v126
	v_rcp_f32_e32 v127, v127
	v_rcp_f32_e32 v128, v128
	v_rcp_f32_e32 v129, v129
	v_rcp_f32_e32 v130, v130
	v_rcp_f32_e32 v131, v131
	v_rcp_f32_e32 v132, v132
	v_rcp_f32_e32 v133, v133
	v_pk_mul_f32 v[118:119], v[118:119], v[126:127]
	v_pk_mul_f32 v[114:115], v[114:115], v[128:129]
	v_pk_mul_f32 v[120:121], v[120:121], v[130:131]
	v_pk_mul_f32 v[116:117], v[116:117], v[132:133]
.LBB0_309:
	v_cvt_pk_bf16_f32 v118, v118, v119
	v_cvt_pk_bf16_f32 v119, v120, v121
	v_cvt_pk_bf16_f32 v120, v114, v115
	v_pk_mul_f32 v[112:113], v[112:113], s[10:11] op_sel_hi:[1,0]
	v_pk_mul_f32 v[110:111], v[110:111], s[10:11] op_sel_hi:[1,0]
	v_pk_mul_f32 v[108:109], v[108:109], s[10:11] op_sel_hi:[1,0]
	s_and_b64 vcc, exec, s[4:5]
	v_pk_mul_f32 v[114:115], v[106:107], s[10:11] op_sel_hi:[1,0]
	v_cvt_pk_bf16_f32 v121, v116, v117
	global_store_dwordx4 v[124:125], v[118:121], off offset:256
	s_cbranch_vccnz .LBB0_311
	s_mov_b32 s98, 0xbdd2d3e7
	s_mov_b32 s100, 0xc0135761
	v_pk_mul_f32 v[106:107], v[110:111], s[98:99] op_sel_hi:[1,0]
	v_pk_mul_f32 v[116:117], v[114:115], s[98:99] op_sel_hi:[1,0]
	v_pk_mul_f32 v[118:119], v[112:113], s[98:99] op_sel_hi:[1,0]
	v_pk_mul_f32 v[120:121], v[108:109], s[98:99] op_sel_hi:[1,0]
	v_pk_fma_f32 v[106:107], v[106:107], v[110:111], s[100:101] op_sel_hi:[1,1,0]
	v_pk_fma_f32 v[116:117], v[116:117], v[114:115], s[100:101] op_sel_hi:[1,1,0]
	v_pk_fma_f32 v[118:119], v[118:119], v[112:113], s[100:101] op_sel_hi:[1,1,0]
	v_pk_fma_f32 v[120:121], v[120:121], v[108:109], s[100:101] op_sel_hi:[1,1,0]
	v_pk_mul_f32 v[106:107], v[106:107], v[110:111]
	v_pk_mul_f32 v[116:117], v[116:117], v[114:115]
	v_pk_mul_f32 v[118:119], v[118:119], v[112:113]
	v_pk_mul_f32 v[120:121], v[120:121], v[108:109]
	v_exp_f32_e32 v106, v106
	v_exp_f32_e32 v107, v107
	v_exp_f32_e32 v116, v116
	v_exp_f32_e32 v117, v117
	v_exp_f32_e32 v118, v118
	v_exp_f32_e32 v119, v119
	v_exp_f32_e32 v120, v120
	v_exp_f32_e32 v121, v121
	v_add_f32_e32 v106, 1.0, v106
	v_add_f32_e32 v107, 1.0, v107
	v_add_f32_e32 v116, 1.0, v116
	v_add_f32_e32 v117, 1.0, v117
	v_add_f32_e32 v118, 1.0, v118
	v_add_f32_e32 v119, 1.0, v119
	v_add_f32_e32 v120, 1.0, v120
	v_add_f32_e32 v121, 1.0, v121
	v_rcp_f32_e32 v106, v106
	v_rcp_f32_e32 v107, v107
	v_rcp_f32_e32 v116, v116
	v_rcp_f32_e32 v117, v117
	v_rcp_f32_e32 v118, v118
	v_rcp_f32_e32 v119, v119
	v_rcp_f32_e32 v120, v120
	v_rcp_f32_e32 v121, v121
	v_pk_mul_f32 v[110:111], v[110:111], v[106:107]
	v_pk_mul_f32 v[114:115], v[114:115], v[116:117]
	v_pk_mul_f32 v[112:113], v[112:113], v[118:119]
	v_pk_mul_f32 v[108:109], v[108:109], v[120:121]
; __device__ __forceinline__ unsigned cvt_pk_bf16(float lo, float hi) { unsigned r; asm volatile("v_cvt_pk_bf16_f32 %0, %1, %2" : "=v"(r) : "v"(lo), "v"(hi)); return r; }
; __device__ __forceinline__ void st_wt16(void* p, u32x4 v) { asm volatile("global_store_dwordx4 %0, %1, off sc1\n\ts_nop 1" :: "v"(p), "v"(v) : "memory"); }
; __device__ __forceinline__ float gelu_tanh(float x) {
;     const float u2 = 1.5957691216057308f * (x + 0.044715f * x * x * x);
;     return x * __builtin_amdgcn_rcpf(1.0f + __expf(-u2));
; }
;     __device__ __forceinline__ void operator()(const f32x4 (&acc)[2][2][4][2], const Unit& u, int wr, int wc, int fr, int fq) const {
;     ...
; #pragma unroll
;         for (int ai = 0; ai < 2; ++ai)
; #pragma unroll
;             for (int m = 0; m < 4; ++m) {
;                 const int row = row0 + ai * HALF + m * 16;
;                 const float rs = rsv[ai * 4 + m];
;                 bf16* rowp = O + (size_t)row * ldc + col0;
; #pragma unroll
;                 for (int bj = 0; bj < 2; ++bj) {
;                     f32x4 v0 = acc[ai][bj][m][0] * rs, v1 = acc[ai][bj][m][1] * rs;
;                     if (gl) {
; #pragma unroll
;                         for (int j = 0; j < 4; ++j) { v0[j] = gelu_tanh(v0[j]); v1[j] = gelu_tanh(v1[j]); }
;                     }
;                     u32x4 w; w.x = cvt_pk_bf16(v0[0], v0[1]); w.y = cvt_pk_bf16(v0[2], v0[3]); w.z = cvt_pk_bf16(v1[0], v1[1]); w.w = cvt_pk_bf16(v1[2], v1[3]);
;                     if (ready && wt) st_wt16(rowp + bj * HALF, w); else *(u32x4*)(rowp + bj * HALF) = w;
.LBB0_311:
	v_or_b32_e32 v116, 16, v64
	v_mov_b64_e32 v[106:107], s[8:9]
	v_mad_i64_i32 v[106:107], s[0:1], v116, s60, v[106:107]
	v_lshl_add_u64 v[106:107], v[122:123], 1, v[106:107]
	v_pk_mul_f32 v[104:105], v[104:105], s[10:11] op_sel_hi:[1,0]
	v_pk_mul_f32 v[102:103], v[102:103], s[10:11] op_sel_hi:[1,0]
	v_pk_mul_f32 v[100:101], v[100:101], s[10:11] op_sel_hi:[1,0]
	s_and_b64 vcc, exec, s[4:5]
	v_pk_mul_f32 v[98:99], v[98:99], s[10:11] op_sel_hi:[1,0]
	v_cvt_pk_bf16_f32 v110, v110, v111
	v_cvt_pk_bf16_f32 v111, v112, v113
	v_cvt_pk_bf16_f32 v112, v114, v115
	v_cvt_pk_bf16_f32 v113, v108, v109
	global_store_dwordx4 v[106:107], v[110:113], off
	s_cbranch_vccnz .LBB0_313
	s_mov_b32 s98, 0xbdd2d3e7
	s_mov_b32 s100, 0xc0135761
	v_pk_mul_f32 v[108:109], v[102:103], s[98:99] op_sel_hi:[1,0]
	v_pk_mul_f32 v[110:111], v[98:99], s[98:99] op_sel_hi:[1,0]
	v_pk_mul_f32 v[112:113], v[104:105], s[98:99] op_sel_hi:[1,0]
	v_pk_mul_f32 v[114:115], v[100:101], s[98:99] op_sel_hi:[1,0]
	v_pk_fma_f32 v[108:109], v[108:109], v[102:103], s[100:101] op_sel_hi:[1,1,0]
	v_pk_fma_f32 v[110:111], v[110:111], v[98:99], s[100:101] op_sel_hi:[1,1,0]
	v_pk_fma_f32 v[112:113], v[112:113], v[104:105], s[100:101] op_sel_hi:[1,1,0]
	v_pk_fma_f32 v[114:115], v[114:115], v[100:101], s[100:101] op_sel_hi:[1,1,0]
	v_pk_mul_f32 v[108:109], v[108:109], v[102:103]
	v_pk_mul_f32 v[110:111], v[110:111], v[98:99]
	v_pk_mul_f32 v[112:113], v[112:113], v[104:105]
	v_pk_mul_f32 v[114:115], v[114:115], v[100:101]
	v_exp_f32_e32 v108, v108
	v_exp_f32_e32 v109, v109
	v_exp_f32_e32 v110, v110
	v_exp_f32_e32 v111, v111
	v_exp_f32_e32 v112, v112
	v_exp_f32_e32 v113, v113
	v_exp_f32_e32 v114, v114
	v_exp_f32_e32 v115, v115
	v_add_f32_e32 v108, 1.0, v108
	v_add_f32_e32 v109, 1.0, v109
	v_add_f32_e32 v110, 1.0, v110
	v_add_f32_e32 v111, 1.0, v111
	v_add_f32_e32 v112, 1.0, v112
	v_add_f32_e32 v113, 1.0, v113
	v_add_f32_e32 v114, 1.0, v114
	v_add_f32_e32 v115, 1.0, v115
	v_rcp_f32_e32 v108, v108
	v_rcp_f32_e32 v109, v109
	v_rcp_f32_e32 v110, v110
	v_rcp_f32_e32 v111, v111
	v_rcp_f32_e32 v112, v112
	v_rcp_f32_e32 v113, v113
	v_rcp_f32_e32 v114, v114
	v_rcp_f32_e32 v115, v115
	v_pk_mul_f32 v[102:103], v[102:103], v[108:109]
	v_pk_mul_f32 v[98:99], v[98:99], v[110:111]
	v_pk_mul_f32 v[104:105], v[104:105], v[112:113]
	v_pk_mul_f32 v[100:101], v[100:101], v[114:115]
.LBB0_313:
	v_cvt_pk_bf16_f32 v102, v102, v103
	v_cvt_pk_bf16_f32 v103, v104, v105
	v_cvt_pk_bf16_f32 v104, v98, v99
	v_pk_mul_f32 v[96:97], v[96:97], s[10:11] op_sel_hi:[1,0]
	v_pk_mul_f32 v[94:95], v[94:95], s[10:11] op_sel_hi:[1,0]
	v_pk_mul_f32 v[92:93], v[92:93], s[10:11] op_sel_hi:[1,0]
	s_and_b64 vcc, exec, s[4:5]
	v_pk_mul_f32 v[98:99], v[90:91], s[10:11] op_sel_hi:[1,0]
	v_cvt_pk_bf16_f32 v105, v100, v101
	global_store_dwordx4 v[106:107], v[102:105], off offset:256
	s_cbranch_vccnz .LBB0_315
	s_mov_b32 s98, 0xbdd2d3e7
	s_mov_b32 s100, 0xc0135761
	v_pk_mul_f32 v[90:91], v[94:95], s[98:99] op_sel_hi:[1,0]
	v_pk_mul_f32 v[100:101], v[98:99], s[98:99] op_sel_hi:[1,0]
	v_pk_mul_f32 v[102:103], v[96:97], s[98:99] op_sel_hi:[1,0]
	v_pk_mul_f32 v[104:105], v[92:93], s[98:99] op_sel_hi:[1,0]
	v_pk_fma_f32 v[90:91], v[90:91], v[94:95], s[100:101] op_sel_hi:[1,1,0]
	v_pk_fma_f32 v[100:101], v[100:101], v[98:99], s[100:101] op_sel_hi:[1,1,0]
	v_pk_fma_f32 v[102:103], v[102:103], v[96:97], s[100:101] op_sel_hi:[1,1,0]
	v_pk_fma_f32 v[104:105], v[104:105], v[92:93], s[100:101] op_sel_hi:[1,1,0]
	v_pk_mul_f32 v[90:91], v[90:91], v[94:95]
	v_pk_mul_f32 v[100:101], v[100:101], v[98:99]
	v_pk_mul_f32 v[102:103], v[102:103], v[96:97]
	v_pk_mul_f32 v[104:105], v[104:105], v[92:93]
	v_exp_f32_e32 v90, v90
	v_exp_f32_e32 v91, v91
	v_exp_f32_e32 v100, v100
	v_exp_f32_e32 v101, v101
	v_exp_f32_e32 v102, v102
	v_exp_f32_e32 v103, v103
	v_exp_f32_e32 v104, v104
	v_exp_f32_e32 v105, v105
	v_add_f32_e32 v90, 1.0, v90
	v_add_f32_e32 v91, 1.0, v91
	v_add_f32_e32 v100, 1.0, v100
	v_add_f32_e32 v101, 1.0, v101
	v_add_f32_e32 v102, 1.0, v102
	v_add_f32_e32 v103, 1.0, v103
	v_add_f32_e32 v104, 1.0, v104
	v_add_f32_e32 v105, 1.0, v105
	v_rcp_f32_e32 v90, v90
	v_rcp_f32_e32 v91, v91
	v_rcp_f32_e32 v100, v100
	v_rcp_f32_e32 v101, v101
	v_rcp_f32_e32 v102, v102
	v_rcp_f32_e32 v103, v103
	v_rcp_f32_e32 v104, v104
	v_rcp_f32_e32 v105, v105
	v_pk_mul_f32 v[94:95], v[94:95], v[90:91]
	v_pk_mul_f32 v[98:99], v[98:99], v[100:101]
	v_pk_mul_f32 v[96:97], v[96:97], v[102:103]
	v_pk_mul_f32 v[92:93], v[92:93], v[104:105]
.LBB0_315:
	v_or_b32_e32 v100, 32, v64
	v_mov_b64_e32 v[90:91], s[8:9]
	v_mad_i64_i32 v[90:91], s[0:1], v100, s60, v[90:91]
	v_lshl_add_u64 v[90:91], v[122:123], 1, v[90:91]
	v_pk_mul_f32 v[88:89], v[88:89], s[10:11] op_sel_hi:[1,0]
	v_pk_mul_f32 v[86:87], v[86:87], s[10:11] op_sel_hi:[1,0]
	v_pk_mul_f32 v[84:85], v[84:85], s[10:11] op_sel_hi:[1,0]
	s_and_b64 vcc, exec, s[4:5]
	v_pk_mul_f32 v[82:83], v[82:83], s[10:11] op_sel_hi:[1,0]
	v_cvt_pk_bf16_f32 v94, v94, v95
	v_cvt_pk_bf16_f32 v95, v96, v97
	v_cvt_pk_bf16_f32 v96, v98, v99
	v_cvt_pk_bf16_f32 v97, v92, v93
	global_store_dwordx4 v[90:91], v[94:97], off
	s_cbranch_vccnz .LBB0_317
	s_mov_b32 s98, 0xbdd2d3e7
	s_mov_b32 s100, 0xc0135761
	v_pk_mul_f32 v[92:93], v[86:87], s[98:99] op_sel_hi:[1,0]
	v_pk_mul_f32 v[94:95], v[82:83], s[98:99] op_sel_hi:[1,0]
	v_pk_mul_f32 v[96:97], v[88:89], s[98:99] op_sel_hi:[1,0]
	v_pk_mul_f32 v[98:99], v[84:85], s[98:99] op_sel_hi:[1,0]
	v_pk_fma_f32 v[92:93], v[92:93], v[86:87], s[100:101] op_sel_hi:[1,1,0]
	v_pk_fma_f32 v[94:95], v[94:95], v[82:83], s[100:101] op_sel_hi:[1,1,0]
	v_pk_fma_f32 v[96:97], v[96:97], v[88:89], s[100:101] op_sel_hi:[1,1,0]
	v_pk_fma_f32 v[98:99], v[98:99], v[84:85], s[100:101] op_sel_hi:[1,1,0]
	v_pk_mul_f32 v[92:93], v[92:93], v[86:87]
	v_pk_mul_f32 v[94:95], v[94:95], v[82:83]
	v_pk_mul_f32 v[96:97], v[96:97], v[88:89]
	v_pk_mul_f32 v[98:99], v[98:99], v[84:85]
	v_exp_f32_e32 v92, v92
	v_exp_f32_e32 v93, v93
	v_exp_f32_e32 v94, v94
	v_exp_f32_e32 v95, v95
	v_exp_f32_e32 v96, v96
	v_exp_f32_e32 v97, v97
	v_exp_f32_e32 v98, v98
	v_exp_f32_e32 v99, v99
	v_add_f32_e32 v92, 1.0, v92
	v_add_f32_e32 v93, 1.0, v93
	v_add_f32_e32 v94, 1.0, v94
	v_add_f32_e32 v95, 1.0, v95
	v_add_f32_e32 v96, 1.0, v96
	v_add_f32_e32 v97, 1.0, v97
	v_add_f32_e32 v98, 1.0, v98
	v_add_f32_e32 v99, 1.0, v99
	v_rcp_f32_e32 v92, v92
	v_rcp_f32_e32 v93, v93
	v_rcp_f32_e32 v94, v94
	v_rcp_f32_e32 v95, v95
	v_rcp_f32_e32 v96, v96
	v_rcp_f32_e32 v97, v97
	v_rcp_f32_e32 v98, v98
	v_rcp_f32_e32 v99, v99
	v_pk_mul_f32 v[86:87], v[86:87], v[92:93]
	v_pk_mul_f32 v[82:83], v[82:83], v[94:95]
	v_pk_mul_f32 v[88:89], v[88:89], v[96:97]
	v_pk_mul_f32 v[84:85], v[84:85], v[98:99]
; __device__ __forceinline__ unsigned cvt_pk_bf16(float lo, float hi) { unsigned r; asm volatile("v_cvt_pk_bf16_f32 %0, %1, %2" : "=v"(r) : "v"(lo), "v"(hi)); return r; }
; __device__ __forceinline__ void st_wt16(void* p, u32x4 v) { asm volatile("global_store_dwordx4 %0, %1, off sc1\n\ts_nop 1" :: "v"(p), "v"(v) : "memory"); }
; __device__ __forceinline__ float gelu_tanh(float x) {
;     const float u2 = 1.5957691216057308f * (x + 0.044715f * x * x * x);
;     return x * __builtin_amdgcn_rcpf(1.0f + __expf(-u2));
; }
;     __device__ __forceinline__ void operator()(const f32x4 (&acc)[2][2][4][2], const Unit& u, int wr, int wc, int fr, int fq) const {
;     ...
; #pragma unroll
;         for (int ai = 0; ai < 2; ++ai)
; #pragma unroll
;             for (int m = 0; m < 4; ++m) {
;                 const int row = row0 + ai * HALF + m * 16;
;                 const float rs = rsv[ai * 4 + m];
;                 bf16* rowp = O + (size_t)row * ldc + col0;
; #pragma unroll
;                 for (int bj = 0; bj < 2; ++bj) {
;                     f32x4 v0 = acc[ai][bj][m][0] * rs, v1 = acc[ai][bj][m][1] * rs;
;                     if (gl) {
; #pragma unroll
;                         for (int j = 0; j < 4; ++j) { v0[j] = gelu_tanh(v0[j]); v1[j] = gelu_tanh(v1[j]); }
;                     }
;                     u32x4 w; w.x = cvt_pk_bf16(v0[0], v0[1]); w.y = cvt_pk_bf16(v0[2], v0[3]); w.z = cvt_pk_bf16(v1[0], v1[1]); w.w = cvt_pk_bf16(v1[2], v1[3]);
;                     if (ready && wt) st_wt16(rowp + bj * HALF, w); else *(u32x4*)(rowp + bj * HALF) = w;
.LBB0_317:
	v_cvt_pk_bf16_f32 v86, v86, v87
	v_cvt_pk_bf16_f32 v87, v88, v89
	v_cvt_pk_bf16_f32 v88, v82, v83
	v_pk_mul_f32 v[80:81], v[80:81], s[10:11] op_sel_hi:[1,0]
	v_pk_mul_f32 v[78:79], v[78:79], s[10:11] op_sel_hi:[1,0]
	v_pk_mul_f32 v[76:77], v[76:77], s[10:11] op_sel_hi:[1,0]
	s_and_b64 vcc, exec, s[4:5]
	v_pk_mul_f32 v[82:83], v[74:75], s[10:11] op_sel_hi:[1,0]
	v_cvt_pk_bf16_f32 v89, v84, v85
	global_store_dwordx4 v[90:91], v[86:89], off offset:256
	s_cbranch_vccnz .LBB0_319
	s_mov_b32 s98, 0xbdd2d3e7
	s_mov_b32 s100, 0xc0135761
	v_pk_mul_f32 v[74:75], v[78:79], s[98:99] op_sel_hi:[1,0]
	v_pk_mul_f32 v[84:85], v[82:83], s[98:99] op_sel_hi:[1,0]
	v_pk_mul_f32 v[86:87], v[80:81], s[98:99] op_sel_hi:[1,0]
	v_pk_mul_f32 v[88:89], v[76:77], s[98:99] op_sel_hi:[1,0]
	v_pk_fma_f32 v[74:75], v[74:75], v[78:79], s[100:101] op_sel_hi:[1,1,0]
	v_pk_fma_f32 v[84:85], v[84:85], v[82:83], s[100:101] op_sel_hi:[1,1,0]
	v_pk_fma_f32 v[86:87], v[86:87], v[80:81], s[100:101] op_sel_hi:[1,1,0]
	v_pk_fma_f32 v[88:89], v[88:89], v[76:77], s[100:101] op_sel_hi:[1,1,0]
	v_pk_mul_f32 v[74:75], v[74:75], v[78:79]
	v_pk_mul_f32 v[84:85], v[84:85], v[82:83]
	v_pk_mul_f32 v[86:87], v[86:87], v[80:81]
	v_pk_mul_f32 v[88:89], v[88:89], v[76:77]
	v_exp_f32_e32 v74, v74
	v_exp_f32_e32 v75, v75
	v_exp_f32_e32 v84, v84
	v_exp_f32_e32 v85, v85
	v_exp_f32_e32 v86, v86
	v_exp_f32_e32 v87, v87
	v_exp_f32_e32 v88, v88
	v_exp_f32_e32 v89, v89
	v_add_f32_e32 v74, 1.0, v74
	v_add_f32_e32 v75, 1.0, v75
	v_add_f32_e32 v84, 1.0, v84
	v_add_f32_e32 v85, 1.0, v85
	v_add_f32_e32 v86, 1.0, v86
	v_add_f32_e32 v87, 1.0, v87
	v_add_f32_e32 v88, 1.0, v88
	v_add_f32_e32 v89, 1.0, v89
	v_rcp_f32_e32 v74, v74
	v_rcp_f32_e32 v75, v75
	v_rcp_f32_e32 v84, v84
	v_rcp_f32_e32 v85, v85
	v_rcp_f32_e32 v86, v86
	v_rcp_f32_e32 v87, v87
	v_rcp_f32_e32 v88, v88
	v_rcp_f32_e32 v89, v89
	v_pk_mul_f32 v[78:79], v[78:79], v[74:75]
	v_pk_mul_f32 v[82:83], v[82:83], v[84:85]
	v_pk_mul_f32 v[80:81], v[80:81], v[86:87]
	v_pk_mul_f32 v[76:77], v[76:77], v[88:89]
.LBB0_319:
	v_or_b32_e32 v84, 48, v64
	v_mov_b64_e32 v[74:75], s[8:9]
	v_mad_i64_i32 v[74:75], s[0:1], v84, s60, v[74:75]
	v_lshl_add_u64 v[74:75], v[122:123], 1, v[74:75]
	v_pk_mul_f32 v[72:73], v[72:73], s[10:11] op_sel_hi:[1,0]
	v_pk_mul_f32 v[70:71], v[70:71], s[10:11] op_sel_hi:[1,0]
	v_pk_mul_f32 v[68:69], v[68:69], s[10:11] op_sel_hi:[1,0]
	s_and_b64 vcc, exec, s[4:5]
	v_pk_mul_f32 v[66:67], v[66:67], s[10:11] op_sel_hi:[1,0]
	v_cvt_pk_bf16_f32 v78, v78, v79
	v_cvt_pk_bf16_f32 v79, v80, v81
	v_cvt_pk_bf16_f32 v80, v82, v83
	v_cvt_pk_bf16_f32 v81, v76, v77
	global_store_dwordx4 v[74:75], v[78:81], off
	s_cbranch_vccnz .LBB0_321
	s_mov_b32 s98, 0xbdd2d3e7
	s_mov_b32 s100, 0xc0135761
	v_pk_mul_f32 v[76:77], v[70:71], s[98:99] op_sel_hi:[1,0]
	v_pk_mul_f32 v[78:79], v[66:67], s[98:99] op_sel_hi:[1,0]
	v_pk_mul_f32 v[80:81], v[72:73], s[98:99] op_sel_hi:[1,0]
	v_pk_mul_f32 v[82:83], v[68:69], s[98:99] op_sel_hi:[1,0]
	v_pk_fma_f32 v[76:77], v[76:77], v[70:71], s[100:101] op_sel_hi:[1,1,0]
	v_pk_fma_f32 v[78:79], v[78:79], v[66:67], s[100:101] op_sel_hi:[1,1,0]
	v_pk_fma_f32 v[80:81], v[80:81], v[72:73], s[100:101] op_sel_hi:[1,1,0]
	v_pk_fma_f32 v[82:83], v[82:83], v[68:69], s[100:101] op_sel_hi:[1,1,0]
	v_pk_mul_f32 v[76:77], v[76:77], v[70:71]
	v_pk_mul_f32 v[78:79], v[78:79], v[66:67]
	v_pk_mul_f32 v[80:81], v[80:81], v[72:73]
	v_pk_mul_f32 v[82:83], v[82:83], v[68:69]
	v_exp_f32_e32 v76, v76
	v_exp_f32_e32 v77, v77
	v_exp_f32_e32 v78, v78
	v_exp_f32_e32 v79, v79
	v_exp_f32_e32 v80, v80
	v_exp_f32_e32 v81, v81
	v_exp_f32_e32 v82, v82
	v_exp_f32_e32 v83, v83
	v_add_f32_e32 v76, 1.0, v76
	v_add_f32_e32 v77, 1.0, v77
	v_add_f32_e32 v78, 1.0, v78
	v_add_f32_e32 v79, 1.0, v79
	v_add_f32_e32 v80, 1.0, v80
	v_add_f32_e32 v81, 1.0, v81
	v_add_f32_e32 v82, 1.0, v82
	v_add_f32_e32 v83, 1.0, v83
	v_rcp_f32_e32 v76, v76
	v_rcp_f32_e32 v77, v77
	v_rcp_f32_e32 v78, v78
	v_rcp_f32_e32 v79, v79
	v_rcp_f32_e32 v80, v80
	v_rcp_f32_e32 v81, v81
	v_rcp_f32_e32 v82, v82
	v_rcp_f32_e32 v83, v83
	v_pk_mul_f32 v[70:71], v[70:71], v[76:77]
	v_pk_mul_f32 v[66:67], v[66:67], v[78:79]
	v_pk_mul_f32 v[72:73], v[72:73], v[80:81]
	v_pk_mul_f32 v[68:69], v[68:69], v[82:83]
.LBB0_321:
	v_cvt_pk_bf16_f32 v70, v70, v71
	v_cvt_pk_bf16_f32 v71, v72, v73
	v_cvt_pk_bf16_f32 v72, v66, v67
	v_pk_mul_f32 v[62:63], v[62:63], s[10:11] op_sel_hi:[1,0]
	v_pk_mul_f32 v[60:61], v[60:61], s[10:11] op_sel_hi:[1,0]
	v_pk_mul_f32 v[58:59], v[58:59], s[10:11] op_sel_hi:[1,0]
	s_and_b64 vcc, exec, s[4:5]
	v_pk_mul_f32 v[66:67], v[56:57], s[10:11] op_sel_hi:[1,0]
	v_cvt_pk_bf16_f32 v73, v68, v69
	global_store_dwordx4 v[74:75], v[70:73], off offset:256
	s_cbranch_vccnz .LBB0_323
	s_mov_b32 s98, 0xbdd2d3e7
	s_mov_b32 s100, 0xc0135761
	v_pk_mul_f32 v[56:57], v[60:61], s[98:99] op_sel_hi:[1,0]
	v_pk_mul_f32 v[68:69], v[66:67], s[98:99] op_sel_hi:[1,0]
	v_pk_mul_f32 v[70:71], v[62:63], s[98:99] op_sel_hi:[1,0]
	v_pk_mul_f32 v[72:73], v[58:59], s[98:99] op_sel_hi:[1,0]
	v_pk_fma_f32 v[56:57], v[56:57], v[60:61], s[100:101] op_sel_hi:[1,1,0]
	v_pk_fma_f32 v[68:69], v[68:69], v[66:67], s[100:101] op_sel_hi:[1,1,0]
	v_pk_fma_f32 v[70:71], v[70:71], v[62:63], s[100:101] op_sel_hi:[1,1,0]
	v_pk_fma_f32 v[72:73], v[72:73], v[58:59], s[100:101] op_sel_hi:[1,1,0]
	v_pk_mul_f32 v[56:57], v[56:57], v[60:61]
	v_pk_mul_f32 v[68:69], v[68:69], v[66:67]
	v_pk_mul_f32 v[70:71], v[70:71], v[62:63]
	v_pk_mul_f32 v[72:73], v[72:73], v[58:59]
	v_exp_f32_e32 v56, v56
	v_exp_f32_e32 v57, v57
	v_exp_f32_e32 v68, v68
	v_exp_f32_e32 v69, v69
	v_exp_f32_e32 v70, v70
	v_exp_f32_e32 v71, v71
	v_exp_f32_e32 v72, v72
	v_exp_f32_e32 v73, v73
	v_add_f32_e32 v56, 1.0, v56
	v_add_f32_e32 v57, 1.0, v57
	v_add_f32_e32 v68, 1.0, v68
	v_add_f32_e32 v69, 1.0, v69
	v_add_f32_e32 v70, 1.0, v70
	v_add_f32_e32 v71, 1.0, v71
	v_add_f32_e32 v72, 1.0, v72
	v_add_f32_e32 v73, 1.0, v73
	v_rcp_f32_e32 v56, v56
	v_rcp_f32_e32 v57, v57
	v_rcp_f32_e32 v68, v68
	v_rcp_f32_e32 v69, v69
	v_rcp_f32_e32 v70, v70
	v_rcp_f32_e32 v71, v71
	v_rcp_f32_e32 v72, v72
	v_rcp_f32_e32 v73, v73
	v_pk_mul_f32 v[60:61], v[60:61], v[56:57]
	v_pk_mul_f32 v[66:67], v[66:67], v[68:69]
	v_pk_mul_f32 v[62:63], v[62:63], v[70:71]
	v_pk_mul_f32 v[58:59], v[58:59], v[72:73]
; __device__ __forceinline__ unsigned cvt_pk_bf16(float lo, float hi) { unsigned r; asm volatile("v_cvt_pk_bf16_f32 %0, %1, %2" : "=v"(r) : "v"(lo), "v"(hi)); return r; }
; __device__ __forceinline__ void st_wt16(void* p, u32x4 v) { asm volatile("global_store_dwordx4 %0, %1, off sc1\n\ts_nop 1" :: "v"(p), "v"(v) : "memory"); }
; __device__ __forceinline__ float gelu_tanh(float x) {
;     const float u2 = 1.5957691216057308f * (x + 0.044715f * x * x * x);
;     return x * __builtin_amdgcn_rcpf(1.0f + __expf(-u2));
; }
;     __device__ __forceinline__ void operator()(const f32x4 (&acc)[2][2][4][2], const Unit& u, int wr, int wc, int fr, int fq) const {
;     ...
;         float rsv[8];
; #pragma unroll
;         for (int j = 0; j < 8; ++j) { const int rw = row0 + (j >> 2) * HALF + (j & 3) * 16; rsv[j] = cs * (rslds ? rslds[rw - u.pm * BM] : (rsrow ? rsrow[rw] : (ssqp ? row_rs(ssqp, rw, fq) : 1.0f))); }
; #pragma unroll
;         for (int ai = 0; ai < 2; ++ai)
; #pragma unroll
;             for (int m = 0; m < 4; ++m) {
;                 const int row = row0 + ai * HALF + m * 16;
;                 const float rs = rsv[ai * 4 + m];
;                 bf16* rowp = O + (size_t)row * ldc + col0;
; #pragma unroll
;                 for (int bj = 0; bj < 2; ++bj) {
;                     f32x4 v0 = acc[ai][bj][m][0] * rs, v1 = acc[ai][bj][m][1] * rs;
;                     if (gl) {
; #pragma unroll
;                         for (int j = 0; j < 4; ++j) { v0[j] = gelu_tanh(v0[j]); v1[j] = gelu_tanh(v1[j]); }
;                     }
;                     u32x4 w; w.x = cvt_pk_bf16(v0[0], v0[1]); w.y = cvt_pk_bf16(v0[2], v0[3]); w.z = cvt_pk_bf16(v1[0], v1[1]); w.w = cvt_pk_bf16(v1[2], v1[3]);
;                     if (ready && wt) st_wt16(rowp + bj * HALF, w); else *(u32x4*)(rowp + bj * HALF) = w;
.LBB0_323:
	v_add_u32_e32 v68, 0x80, v64
	v_mov_b64_e32 v[56:57], s[8:9]
	v_mad_i64_i32 v[56:57], s[0:1], v68, s60, v[56:57]
	v_lshl_add_u64 v[56:57], v[122:123], 1, v[56:57]
	v_pk_mul_f32 v[54:55], v[54:55], s[10:11] op_sel_hi:[1,0]
	v_pk_mul_f32 v[52:53], v[52:53], s[10:11] op_sel_hi:[1,0]
	v_pk_mul_f32 v[50:51], v[50:51], s[10:11] op_sel_hi:[1,0]
	s_and_b64 vcc, exec, s[4:5]
	v_pk_mul_f32 v[48:49], v[48:49], s[10:11] op_sel_hi:[1,0]
	v_cvt_pk_bf16_f32 v60, v60, v61
	v_cvt_pk_bf16_f32 v61, v62, v63
	v_cvt_pk_bf16_f32 v62, v66, v67
	v_cvt_pk_bf16_f32 v63, v58, v59
	global_store_dwordx4 v[56:57], v[60:63], off
	s_cbranch_vccnz .LBB0_325
	s_mov_b32 s98, 0xbdd2d3e7
	s_mov_b32 s100, 0xc0135761
	v_pk_mul_f32 v[58:59], v[52:53], s[98:99] op_sel_hi:[1,0]
	v_pk_mul_f32 v[60:61], v[48:49], s[98:99] op_sel_hi:[1,0]
	v_pk_mul_f32 v[62:63], v[54:55], s[98:99] op_sel_hi:[1,0]
	v_pk_mul_f32 v[66:67], v[50:51], s[98:99] op_sel_hi:[1,0]
	v_pk_fma_f32 v[58:59], v[58:59], v[52:53], s[100:101] op_sel_hi:[1,1,0]
	v_pk_fma_f32 v[60:61], v[60:61], v[48:49], s[100:101] op_sel_hi:[1,1,0]
	v_pk_fma_f32 v[62:63], v[62:63], v[54:55], s[100:101] op_sel_hi:[1,1,0]
	v_pk_fma_f32 v[66:67], v[66:67], v[50:51], s[100:101] op_sel_hi:[1,1,0]
	v_pk_mul_f32 v[58:59], v[58:59], v[52:53]
	v_pk_mul_f32 v[60:61], v[60:61], v[48:49]
	v_pk_mul_f32 v[62:63], v[62:63], v[54:55]
	v_pk_mul_f32 v[66:67], v[66:67], v[50:51]
	v_exp_f32_e32 v58, v58
	v_exp_f32_e32 v59, v59
	v_exp_f32_e32 v60, v60
	v_exp_f32_e32 v61, v61
	v_exp_f32_e32 v62, v62
	v_exp_f32_e32 v63, v63
	v_exp_f32_e32 v66, v66
	v_exp_f32_e32 v67, v67
	v_add_f32_e32 v58, 1.0, v58
	v_add_f32_e32 v59, 1.0, v59
	v_add_f32_e32 v60, 1.0, v60
	v_add_f32_e32 v61, 1.0, v61
	v_add_f32_e32 v62, 1.0, v62
	v_add_f32_e32 v63, 1.0, v63
	v_add_f32_e32 v66, 1.0, v66
	v_add_f32_e32 v67, 1.0, v67
	v_rcp_f32_e32 v58, v58
	v_rcp_f32_e32 v59, v59
	v_rcp_f32_e32 v60, v60
	v_rcp_f32_e32 v61, v61
	v_rcp_f32_e32 v62, v62
	v_rcp_f32_e32 v63, v63
	v_rcp_f32_e32 v66, v66
	v_rcp_f32_e32 v67, v67
	v_pk_mul_f32 v[52:53], v[52:53], v[58:59]
	v_pk_mul_f32 v[48:49], v[48:49], v[60:61]
	v_pk_mul_f32 v[54:55], v[54:55], v[62:63]
	v_pk_mul_f32 v[50:51], v[50:51], v[66:67]
.LBB0_325:
	v_cvt_pk_bf16_f32 v52, v52, v53
	v_cvt_pk_bf16_f32 v53, v54, v55
	v_cvt_pk_bf16_f32 v54, v48, v49
	v_pk_mul_f32 v[46:47], v[46:47], s[10:11] op_sel_hi:[1,0]
	v_pk_mul_f32 v[44:45], v[44:45], s[10:11] op_sel_hi:[1,0]
	v_pk_mul_f32 v[42:43], v[42:43], s[10:11] op_sel_hi:[1,0]
	s_and_b64 vcc, exec, s[4:5]
	v_pk_mul_f32 v[48:49], v[40:41], s[10:11] op_sel_hi:[1,0]
	v_cvt_pk_bf16_f32 v55, v50, v51
	global_store_dwordx4 v[56:57], v[52:55], off offset:256
	s_cbranch_vccnz .LBB0_327
	s_mov_b32 s98, 0xbdd2d3e7
	s_mov_b32 s100, 0xc0135761
	v_pk_mul_f32 v[40:41], v[44:45], s[98:99] op_sel_hi:[1,0]
	v_pk_mul_f32 v[50:51], v[48:49], s[98:99] op_sel_hi:[1,0]
	v_pk_mul_f32 v[52:53], v[46:47], s[98:99] op_sel_hi:[1,0]
	v_pk_mul_f32 v[54:55], v[42:43], s[98:99] op_sel_hi:[1,0]
	v_pk_fma_f32 v[40:41], v[40:41], v[44:45], s[100:101] op_sel_hi:[1,1,0]
	v_pk_fma_f32 v[50:51], v[50:51], v[48:49], s[100:101] op_sel_hi:[1,1,0]
	v_pk_fma_f32 v[52:53], v[52:53], v[46:47], s[100:101] op_sel_hi:[1,1,0]
	v_pk_fma_f32 v[54:55], v[54:55], v[42:43], s[100:101] op_sel_hi:[1,1,0]
	v_pk_mul_f32 v[40:41], v[40:41], v[44:45]
	v_pk_mul_f32 v[50:51], v[50:51], v[48:49]
	v_pk_mul_f32 v[52:53], v[52:53], v[46:47]
	v_pk_mul_f32 v[54:55], v[54:55], v[42:43]
	v_exp_f32_e32 v40, v40
	v_exp_f32_e32 v41, v41
	v_exp_f32_e32 v50, v50
	v_exp_f32_e32 v51, v51
	v_exp_f32_e32 v52, v52
	v_exp_f32_e32 v53, v53
	v_exp_f32_e32 v54, v54
	v_exp_f32_e32 v55, v55
	v_add_f32_e32 v40, 1.0, v40
	v_add_f32_e32 v41, 1.0, v41
	v_add_f32_e32 v50, 1.0, v50
	v_add_f32_e32 v51, 1.0, v51
	v_add_f32_e32 v52, 1.0, v52
	v_add_f32_e32 v53, 1.0, v53
	v_add_f32_e32 v54, 1.0, v54
	v_add_f32_e32 v55, 1.0, v55
	v_rcp_f32_e32 v40, v40
	v_rcp_f32_e32 v41, v41
	v_rcp_f32_e32 v50, v50
	v_rcp_f32_e32 v51, v51
	v_rcp_f32_e32 v52, v52
	v_rcp_f32_e32 v53, v53
	v_rcp_f32_e32 v54, v54
	v_rcp_f32_e32 v55, v55
	v_pk_mul_f32 v[44:45], v[44:45], v[40:41]
	v_pk_mul_f32 v[48:49], v[48:49], v[50:51]
	v_pk_mul_f32 v[46:47], v[46:47], v[52:53]
	v_pk_mul_f32 v[42:43], v[42:43], v[54:55]
.LBB0_327:
	v_add_u32_e32 v50, 0x90, v64
	v_mov_b64_e32 v[40:41], s[8:9]
	v_mad_i64_i32 v[40:41], s[0:1], v50, s60, v[40:41]
	v_lshl_add_u64 v[40:41], v[122:123], 1, v[40:41]
	v_pk_mul_f32 v[38:39], v[38:39], s[10:11] op_sel_hi:[1,0]
	v_pk_mul_f32 v[36:37], v[36:37], s[10:11] op_sel_hi:[1,0]
	v_pk_mul_f32 v[34:35], v[34:35], s[10:11] op_sel_hi:[1,0]
	s_and_b64 vcc, exec, s[4:5]
	v_pk_mul_f32 v[32:33], v[32:33], s[10:11] op_sel_hi:[1,0]
	v_cvt_pk_bf16_f32 v44, v44, v45
	v_cvt_pk_bf16_f32 v45, v46, v47
	v_cvt_pk_bf16_f32 v46, v48, v49
	v_cvt_pk_bf16_f32 v47, v42, v43
	global_store_dwordx4 v[40:41], v[44:47], off
	s_cbranch_vccnz .LBB0_329
	s_mov_b32 s98, 0xbdd2d3e7
	s_mov_b32 s100, 0xc0135761
	v_pk_mul_f32 v[42:43], v[36:37], s[98:99] op_sel_hi:[1,0]
	v_pk_mul_f32 v[44:45], v[32:33], s[98:99] op_sel_hi:[1,0]
	v_pk_mul_f32 v[46:47], v[38:39], s[98:99] op_sel_hi:[1,0]
	v_pk_mul_f32 v[48:49], v[34:35], s[98:99] op_sel_hi:[1,0]
	v_pk_fma_f32 v[42:43], v[42:43], v[36:37], s[100:101] op_sel_hi:[1,1,0]
	v_pk_fma_f32 v[44:45], v[44:45], v[32:33], s[100:101] op_sel_hi:[1,1,0]
	v_pk_fma_f32 v[46:47], v[46:47], v[38:39], s[100:101] op_sel_hi:[1,1,0]
	v_pk_fma_f32 v[48:49], v[48:49], v[34:35], s[100:101] op_sel_hi:[1,1,0]
	v_pk_mul_f32 v[42:43], v[42:43], v[36:37]
	v_pk_mul_f32 v[44:45], v[44:45], v[32:33]
	v_pk_mul_f32 v[46:47], v[46:47], v[38:39]
	v_pk_mul_f32 v[48:49], v[48:49], v[34:35]
	v_exp_f32_e32 v42, v42
	v_exp_f32_e32 v43, v43
	v_exp_f32_e32 v44, v44
	v_exp_f32_e32 v45, v45
	v_exp_f32_e32 v46, v46
	v_exp_f32_e32 v47, v47
	v_exp_f32_e32 v48, v48
	v_exp_f32_e32 v49, v49
	v_add_f32_e32 v42, 1.0, v42
	v_add_f32_e32 v43, 1.0, v43
	v_add_f32_e32 v44, 1.0, v44
	v_add_f32_e32 v45, 1.0, v45
	v_add_f32_e32 v46, 1.0, v46
	v_add_f32_e32 v47, 1.0, v47
	v_add_f32_e32 v48, 1.0, v48
	v_add_f32_e32 v49, 1.0, v49
	v_rcp_f32_e32 v42, v42
	v_rcp_f32_e32 v43, v43
	v_rcp_f32_e32 v44, v44
	v_rcp_f32_e32 v45, v45
	v_rcp_f32_e32 v46, v46
	v_rcp_f32_e32 v47, v47
	v_rcp_f32_e32 v48, v48
	v_rcp_f32_e32 v49, v49
	v_pk_mul_f32 v[36:37], v[36:37], v[42:43]
	v_pk_mul_f32 v[32:33], v[32:33], v[44:45]
	v_pk_mul_f32 v[38:39], v[38:39], v[46:47]
	v_pk_mul_f32 v[34:35], v[34:35], v[48:49]
; __device__ __forceinline__ unsigned cvt_pk_bf16(float lo, float hi) { unsigned r; asm volatile("v_cvt_pk_bf16_f32 %0, %1, %2" : "=v"(r) : "v"(lo), "v"(hi)); return r; }
; __device__ __forceinline__ void st_wt16(void* p, u32x4 v) { asm volatile("global_store_dwordx4 %0, %1, off sc1\n\ts_nop 1" :: "v"(p), "v"(v) : "memory"); }
; __device__ __forceinline__ float gelu_tanh(float x) {
;     const float u2 = 1.5957691216057308f * (x + 0.044715f * x * x * x);
;     return x * __builtin_amdgcn_rcpf(1.0f + __expf(-u2));
; }
;     __device__ __forceinline__ void operator()(const f32x4 (&acc)[2][2][4][2], const Unit& u, int wr, int wc, int fr, int fq) const {
;     ...
;         float rsv[8];
; #pragma unroll
;         for (int j = 0; j < 8; ++j) { const int rw = row0 + (j >> 2) * HALF + (j & 3) * 16; rsv[j] = cs * (rslds ? rslds[rw - u.pm * BM] : (rsrow ? rsrow[rw] : (ssqp ? row_rs(ssqp, rw, fq) : 1.0f))); }
; #pragma unroll
;         for (int ai = 0; ai < 2; ++ai)
; #pragma unroll
;             for (int m = 0; m < 4; ++m) {
;                 const int row = row0 + ai * HALF + m * 16;
;                 const float rs = rsv[ai * 4 + m];
;                 bf16* rowp = O + (size_t)row * ldc + col0;
; #pragma unroll
;                 for (int bj = 0; bj < 2; ++bj) {
;                     f32x4 v0 = acc[ai][bj][m][0] * rs, v1 = acc[ai][bj][m][1] * rs;
;                     if (gl) {
; #pragma unroll
;                         for (int j = 0; j < 4; ++j) { v0[j] = gelu_tanh(v0[j]); v1[j] = gelu_tanh(v1[j]); }
;                     }
;                     u32x4 w; w.x = cvt_pk_bf16(v0[0], v0[1]); w.y = cvt_pk_bf16(v0[2], v0[3]); w.z = cvt_pk_bf16(v1[0], v1[1]); w.w = cvt_pk_bf16(v1[2], v1[3]);
;                     if (ready && wt) st_wt16(rowp + bj * HALF, w); else *(u32x4*)(rowp + bj * HALF) = w;
.LBB0_329:
	v_cvt_pk_bf16_f32 v36, v36, v37
	v_cvt_pk_bf16_f32 v37, v38, v39
	v_cvt_pk_bf16_f32 v38, v32, v33
	v_pk_mul_f32 v[30:31], v[30:31], s[10:11] op_sel_hi:[1,0]
	v_pk_mul_f32 v[28:29], v[28:29], s[10:11] op_sel_hi:[1,0]
	v_pk_mul_f32 v[26:27], v[26:27], s[10:11] op_sel_hi:[1,0]
	s_and_b64 vcc, exec, s[4:5]
	v_pk_mul_f32 v[32:33], v[24:25], s[10:11] op_sel_hi:[1,0]
	v_cvt_pk_bf16_f32 v39, v34, v35
	global_store_dwordx4 v[40:41], v[36:39], off offset:256
	s_cbranch_vccnz .LBB0_331
	s_mov_b32 s98, 0xbdd2d3e7
	s_mov_b32 s100, 0xc0135761
	v_pk_mul_f32 v[24:25], v[28:29], s[98:99] op_sel_hi:[1,0]
	v_pk_mul_f32 v[34:35], v[32:33], s[98:99] op_sel_hi:[1,0]
	v_pk_mul_f32 v[36:37], v[30:31], s[98:99] op_sel_hi:[1,0]
	v_pk_mul_f32 v[38:39], v[26:27], s[98:99] op_sel_hi:[1,0]
	v_pk_fma_f32 v[24:25], v[24:25], v[28:29], s[100:101] op_sel_hi:[1,1,0]
	v_pk_fma_f32 v[34:35], v[34:35], v[32:33], s[100:101] op_sel_hi:[1,1,0]
	v_pk_fma_f32 v[36:37], v[36:37], v[30:31], s[100:101] op_sel_hi:[1,1,0]
	v_pk_fma_f32 v[38:39], v[38:39], v[26:27], s[100:101] op_sel_hi:[1,1,0]
	v_pk_mul_f32 v[24:25], v[24:25], v[28:29]
	v_pk_mul_f32 v[34:35], v[34:35], v[32:33]
	v_pk_mul_f32 v[36:37], v[36:37], v[30:31]
	v_pk_mul_f32 v[38:39], v[38:39], v[26:27]
	v_exp_f32_e32 v24, v24
	v_exp_f32_e32 v25, v25
	v_exp_f32_e32 v34, v34
	v_exp_f32_e32 v35, v35
	v_exp_f32_e32 v36, v36
	v_exp_f32_e32 v37, v37
	v_exp_f32_e32 v38, v38
	v_exp_f32_e32 v39, v39
	v_add_f32_e32 v24, 1.0, v24
	v_add_f32_e32 v25, 1.0, v25
	v_add_f32_e32 v34, 1.0, v34
	v_add_f32_e32 v35, 1.0, v35
	v_add_f32_e32 v36, 1.0, v36
	v_add_f32_e32 v37, 1.0, v37
	v_add_f32_e32 v38, 1.0, v38
	v_add_f32_e32 v39, 1.0, v39
	v_rcp_f32_e32 v24, v24
	v_rcp_f32_e32 v25, v25
	v_rcp_f32_e32 v34, v34
	v_rcp_f32_e32 v35, v35
	v_rcp_f32_e32 v36, v36
	v_rcp_f32_e32 v37, v37
	v_rcp_f32_e32 v38, v38
	v_rcp_f32_e32 v39, v39
	v_pk_mul_f32 v[28:29], v[28:29], v[24:25]
	v_pk_mul_f32 v[32:33], v[32:33], v[34:35]
	v_pk_mul_f32 v[30:31], v[30:31], v[36:37]
	v_pk_mul_f32 v[26:27], v[26:27], v[38:39]
.LBB0_331:
	v_add_u32_e32 v34, 0xa0, v64
	v_mov_b64_e32 v[24:25], s[8:9]
	v_mad_i64_i32 v[24:25], s[0:1], v34, s60, v[24:25]
	v_lshl_add_u64 v[24:25], v[122:123], 1, v[24:25]
	v_pk_mul_f32 v[22:23], v[22:23], s[10:11] op_sel_hi:[1,0]
	v_pk_mul_f32 v[20:21], v[20:21], s[10:11] op_sel_hi:[1,0]
	v_pk_mul_f32 v[18:19], v[18:19], s[10:11] op_sel_hi:[1,0]
	s_and_b64 vcc, exec, s[4:5]
	v_pk_mul_f32 v[16:17], v[16:17], s[10:11] op_sel_hi:[1,0]
	v_cvt_pk_bf16_f32 v28, v28, v29
	v_cvt_pk_bf16_f32 v29, v30, v31
	v_cvt_pk_bf16_f32 v30, v32, v33
	v_cvt_pk_bf16_f32 v31, v26, v27
	global_store_dwordx4 v[24:25], v[28:31], off
	s_cbranch_vccnz .LBB0_333
	s_mov_b32 s98, 0xbdd2d3e7
	s_mov_b32 s100, 0xc0135761
	v_pk_mul_f32 v[26:27], v[20:21], s[98:99] op_sel_hi:[1,0]
	v_pk_mul_f32 v[28:29], v[16:17], s[98:99] op_sel_hi:[1,0]
	v_pk_mul_f32 v[30:31], v[22:23], s[98:99] op_sel_hi:[1,0]
	v_pk_mul_f32 v[32:33], v[18:19], s[98:99] op_sel_hi:[1,0]
	v_pk_fma_f32 v[26:27], v[26:27], v[20:21], s[100:101] op_sel_hi:[1,1,0]
	v_pk_fma_f32 v[28:29], v[28:29], v[16:17], s[100:101] op_sel_hi:[1,1,0]
	v_pk_fma_f32 v[30:31], v[30:31], v[22:23], s[100:101] op_sel_hi:[1,1,0]
	v_pk_fma_f32 v[32:33], v[32:33], v[18:19], s[100:101] op_sel_hi:[1,1,0]
	v_pk_mul_f32 v[26:27], v[26:27], v[20:21]
	v_pk_mul_f32 v[28:29], v[28:29], v[16:17]
	v_pk_mul_f32 v[30:31], v[30:31], v[22:23]
	v_pk_mul_f32 v[32:33], v[32:33], v[18:19]
	v_exp_f32_e32 v26, v26
	v_exp_f32_e32 v27, v27
	v_exp_f32_e32 v28, v28
	v_exp_f32_e32 v29, v29
	v_exp_f32_e32 v30, v30
	v_exp_f32_e32 v31, v31
	v_exp_f32_e32 v32, v32
	v_exp_f32_e32 v33, v33
	v_add_f32_e32 v26, 1.0, v26
	v_add_f32_e32 v27, 1.0, v27
	v_add_f32_e32 v28, 1.0, v28
	v_add_f32_e32 v29, 1.0, v29
	v_add_f32_e32 v30, 1.0, v30
	v_add_f32_e32 v31, 1.0, v31
	v_add_f32_e32 v32, 1.0, v32
	v_add_f32_e32 v33, 1.0, v33
	v_rcp_f32_e32 v26, v26
	v_rcp_f32_e32 v27, v27
	v_rcp_f32_e32 v28, v28
	v_rcp_f32_e32 v29, v29
	v_rcp_f32_e32 v30, v30
	v_rcp_f32_e32 v31, v31
	v_rcp_f32_e32 v32, v32
	v_rcp_f32_e32 v33, v33
	v_pk_mul_f32 v[20:21], v[20:21], v[26:27]
	v_pk_mul_f32 v[16:17], v[16:17], v[28:29]
	v_pk_mul_f32 v[22:23], v[22:23], v[30:31]
	v_pk_mul_f32 v[18:19], v[18:19], v[32:33]
; __device__ __forceinline__ unsigned cvt_pk_bf16(float lo, float hi) { unsigned r; asm volatile("v_cvt_pk_bf16_f32 %0, %1, %2" : "=v"(r) : "v"(lo), "v"(hi)); return r; }
; __device__ __forceinline__ void st_wt16(void* p, u32x4 v) { asm volatile("global_store_dwordx4 %0, %1, off sc1\n\ts_nop 1" :: "v"(p), "v"(v) : "memory"); }
; __device__ __forceinline__ float gelu_tanh(float x) {
;     const float u2 = 1.5957691216057308f * (x + 0.044715f * x * x * x);
;     return x * __builtin_amdgcn_rcpf(1.0f + __expf(-u2));
; }
;     __device__ __forceinline__ void operator()(const f32x4 (&acc)[2][2][4][2], const Unit& u, int wr, int wc, int fr, int fq) const {
;     ...
;         float rsv[8];
; #pragma unroll
;         for (int j = 0; j < 8; ++j) { const int rw = row0 + (j >> 2) * HALF + (j & 3) * 16; rsv[j] = cs * (rslds ? rslds[rw - u.pm * BM] : (rsrow ? rsrow[rw] : (ssqp ? row_rs(ssqp, rw, fq) : 1.0f))); }
; #pragma unroll
;         for (int ai = 0; ai < 2; ++ai)
; #pragma unroll
;             for (int m = 0; m < 4; ++m) {
;                 const int row = row0 + ai * HALF + m * 16;
;                 const float rs = rsv[ai * 4 + m];
;                 bf16* rowp = O + (size_t)row * ldc + col0;
; #pragma unroll
;                 for (int bj = 0; bj < 2; ++bj) {
;                     f32x4 v0 = acc[ai][bj][m][0] * rs, v1 = acc[ai][bj][m][1] * rs;
;                     if (gl) {
; #pragma unroll
;                         for (int j = 0; j < 4; ++j) { v0[j] = gelu_tanh(v0[j]); v1[j] = gelu_tanh(v1[j]); }
;                     }
;                     u32x4 w; w.x = cvt_pk_bf16(v0[0], v0[1]); w.y = cvt_pk_bf16(v0[2], v0[3]); w.z = cvt_pk_bf16(v1[0], v1[1]); w.w = cvt_pk_bf16(v1[2], v1[3]);
;                     if (ready && wt) st_wt16(rowp + bj * HALF, w); else *(u32x4*)(rowp + bj * HALF) = w;
.LBB0_333:
	v_cvt_pk_bf16_f32 v20, v20, v21
	v_cvt_pk_bf16_f32 v21, v22, v23
	v_cvt_pk_bf16_f32 v22, v16, v17
	v_pk_mul_f32 v[14:15], v[14:15], s[10:11] op_sel_hi:[1,0]
	v_pk_mul_f32 v[12:13], v[12:13], s[10:11] op_sel_hi:[1,0]
	v_pk_mul_f32 v[10:11], v[10:11], s[10:11] op_sel_hi:[1,0]
	s_and_b64 vcc, exec, s[4:5]
	v_pk_mul_f32 v[16:17], v[8:9], s[10:11] op_sel_hi:[1,0]
	v_cvt_pk_bf16_f32 v23, v18, v19
	global_store_dwordx4 v[24:25], v[20:23], off offset:256
	s_cbranch_vccnz .LBB0_335
	s_mov_b32 s98, 0xbdd2d3e7
	s_mov_b32 s100, 0xc0135761
	v_pk_mul_f32 v[8:9], v[12:13], s[98:99] op_sel_hi:[1,0]
	v_pk_mul_f32 v[18:19], v[16:17], s[98:99] op_sel_hi:[1,0]
	v_pk_mul_f32 v[20:21], v[14:15], s[98:99] op_sel_hi:[1,0]
	v_pk_mul_f32 v[22:23], v[10:11], s[98:99] op_sel_hi:[1,0]
	v_pk_fma_f32 v[8:9], v[8:9], v[12:13], s[100:101] op_sel_hi:[1,1,0]
	v_pk_fma_f32 v[18:19], v[18:19], v[16:17], s[100:101] op_sel_hi:[1,1,0]
	v_pk_fma_f32 v[20:21], v[20:21], v[14:15], s[100:101] op_sel_hi:[1,1,0]
	v_pk_fma_f32 v[22:23], v[22:23], v[10:11], s[100:101] op_sel_hi:[1,1,0]
	v_pk_mul_f32 v[8:9], v[8:9], v[12:13]
	v_pk_mul_f32 v[18:19], v[18:19], v[16:17]
	v_pk_mul_f32 v[20:21], v[20:21], v[14:15]
	v_pk_mul_f32 v[22:23], v[22:23], v[10:11]
	v_exp_f32_e32 v8, v8
	v_exp_f32_e32 v9, v9
	v_exp_f32_e32 v18, v18
	v_exp_f32_e32 v19, v19
	v_exp_f32_e32 v20, v20
	v_exp_f32_e32 v21, v21
	v_exp_f32_e32 v22, v22
	v_exp_f32_e32 v23, v23
	v_add_f32_e32 v8, 1.0, v8
	v_add_f32_e32 v9, 1.0, v9
	v_add_f32_e32 v18, 1.0, v18
	v_add_f32_e32 v19, 1.0, v19
	v_add_f32_e32 v20, 1.0, v20
	v_add_f32_e32 v21, 1.0, v21
	v_add_f32_e32 v22, 1.0, v22
	v_add_f32_e32 v23, 1.0, v23
	v_rcp_f32_e32 v8, v8
	v_rcp_f32_e32 v9, v9
	v_rcp_f32_e32 v18, v18
	v_rcp_f32_e32 v19, v19
	v_rcp_f32_e32 v20, v20
	v_rcp_f32_e32 v21, v21
	v_rcp_f32_e32 v22, v22
	v_rcp_f32_e32 v23, v23
	v_pk_mul_f32 v[12:13], v[12:13], v[8:9]
	v_pk_mul_f32 v[16:17], v[16:17], v[18:19]
	v_pk_mul_f32 v[14:15], v[14:15], v[20:21]
	v_pk_mul_f32 v[10:11], v[10:11], v[22:23]
.LBB0_335:
	v_add_u32_e32 v18, 0xb0, v64
	v_mov_b64_e32 v[8:9], s[8:9]
	v_mad_i64_i32 v[8:9], s[0:1], v18, s60, v[8:9]
	v_lshl_add_u64 v[8:9], v[122:123], 1, v[8:9]
	v_pk_mul_f32 v[6:7], v[6:7], s[10:11] op_sel_hi:[1,0]
	v_pk_mul_f32 v[4:5], v[4:5], s[10:11] op_sel_hi:[1,0]
	v_pk_mul_f32 v[2:3], v[2:3], s[10:11] op_sel_hi:[1,0]
	s_and_b64 vcc, exec, s[4:5]
	v_pk_mul_f32 v[0:1], v[0:1], s[10:11] op_sel_hi:[1,0]
	v_cvt_pk_bf16_f32 v12, v12, v13
	v_cvt_pk_bf16_f32 v13, v14, v15
	v_cvt_pk_bf16_f32 v14, v16, v17
	v_cvt_pk_bf16_f32 v15, v10, v11
	global_store_dwordx4 v[8:9], v[12:15], off
	s_cbranch_vccnz .LBB0_337
	s_mov_b32 s98, 0xbdd2d3e7
	s_mov_b32 s100, 0xc0135761
	v_pk_mul_f32 v[10:11], v[4:5], s[98:99] op_sel_hi:[1,0]
	v_pk_mul_f32 v[12:13], v[0:1], s[98:99] op_sel_hi:[1,0]
	v_pk_mul_f32 v[14:15], v[6:7], s[98:99] op_sel_hi:[1,0]
	v_pk_mul_f32 v[16:17], v[2:3], s[98:99] op_sel_hi:[1,0]
	v_pk_fma_f32 v[10:11], v[10:11], v[4:5], s[100:101] op_sel_hi:[1,1,0]
	v_pk_fma_f32 v[12:13], v[12:13], v[0:1], s[100:101] op_sel_hi:[1,1,0]
	v_pk_fma_f32 v[14:15], v[14:15], v[6:7], s[100:101] op_sel_hi:[1,1,0]
	v_pk_fma_f32 v[16:17], v[16:17], v[2:3], s[100:101] op_sel_hi:[1,1,0]
	v_pk_mul_f32 v[10:11], v[10:11], v[4:5]
	v_pk_mul_f32 v[12:13], v[12:13], v[0:1]
	v_pk_mul_f32 v[14:15], v[14:15], v[6:7]
	v_pk_mul_f32 v[16:17], v[16:17], v[2:3]
	v_exp_f32_e32 v10, v10
	v_exp_f32_e32 v11, v11
	v_exp_f32_e32 v12, v12
	v_exp_f32_e32 v13, v13
	v_exp_f32_e32 v14, v14
	v_exp_f32_e32 v15, v15
	v_exp_f32_e32 v16, v16
	v_exp_f32_e32 v17, v17
	v_add_f32_e32 v10, 1.0, v10
	v_add_f32_e32 v11, 1.0, v11
	v_add_f32_e32 v12, 1.0, v12
	v_add_f32_e32 v13, 1.0, v13
	v_add_f32_e32 v14, 1.0, v14
	v_add_f32_e32 v15, 1.0, v15
	v_add_f32_e32 v16, 1.0, v16
	v_add_f32_e32 v17, 1.0, v17
	v_rcp_f32_e32 v10, v10
	v_rcp_f32_e32 v11, v11
	v_rcp_f32_e32 v12, v12
	v_rcp_f32_e32 v13, v13
	v_rcp_f32_e32 v14, v14
	v_rcp_f32_e32 v15, v15
	v_rcp_f32_e32 v16, v16
	v_rcp_f32_e32 v17, v17
	v_pk_mul_f32 v[4:5], v[4:5], v[10:11]
	v_pk_mul_f32 v[0:1], v[0:1], v[12:13]
	v_pk_mul_f32 v[6:7], v[6:7], v[14:15]
	v_pk_mul_f32 v[2:3], v[2:3], v[16:17]
